# speedup vs baseline: 1.0125x; 1.0125x over previous
.Lk2_pro_nopsi:
	s_add_u32 s38, s38, 1
	s_cmp_le_u32 s38, 4
	s_cbranch_scc1 .Lk2_pro
	v_accvgpr_write_b32 a0, 0
	v_accvgpr_write_b32 a1, 0
	v_accvgpr_write_b32 a2, 0
	v_accvgpr_write_b32 a3, 0
	v_accvgpr_write_b32 a4, 0
	v_accvgpr_write_b32 a5, 0
	v_accvgpr_write_b32 a6, 0
	v_accvgpr_write_b32 a7, 0
	v_accvgpr_write_b32 a8, 0
	v_accvgpr_write_b32 a9, 0
	v_accvgpr_write_b32 a10, 0
	v_accvgpr_write_b32 a11, 0
	v_accvgpr_write_b32 a12, 0
	v_accvgpr_write_b32 a13, 0
	v_accvgpr_write_b32 a14, 0
	v_accvgpr_write_b32 a15, 0
	v_accvgpr_write_b32 a16, 0
	v_accvgpr_write_b32 a17, 0
	v_accvgpr_write_b32 a18, 0
	v_accvgpr_write_b32 a19, 0
	v_accvgpr_write_b32 a20, 0
	v_accvgpr_write_b32 a21, 0
	v_accvgpr_write_b32 a22, 0
	v_accvgpr_write_b32 a23, 0
	v_accvgpr_write_b32 a24, 0
	v_accvgpr_write_b32 a25, 0
	v_accvgpr_write_b32 a26, 0
	v_accvgpr_write_b32 a27, 0
	v_accvgpr_write_b32 a28, 0
	v_accvgpr_write_b32 a29, 0
	v_accvgpr_write_b32 a30, 0
	v_accvgpr_write_b32 a31, 0
	s_cmp_eq_u32 s46, 0
	s_cbranch_scc1 .Lk2_pro_w6
	s_waitcnt vmcnt(12)
	s_branch .Lk2_pro_bar

.Lk2_b00:
	s_waitcnt lgkmcnt(4)
	v_mfma_f32_32x32x16_f16 a[16:31], v[144:147], v[80:83], a[16:31]
	s_cmp_le_u32 s22, 16
	s_cselect_b32 s40, s18, 0x18000
	s_add_u32 m0, s40, s35
	s_add_u32 s22, s22, 1
	global_load_lds_dwordx4 v168, s[20:21]
	global_load_lds_dwordx4 v168, s[20:21] offset:1024
	v_pk_mul_f16 v152, v48, v32 op_sel:[1,0] op_sel_hi:[1,1]
	v_pk_mul_f16 v153, v48, v33 op_sel:[1,0] op_sel_hi:[1,1]
	v_pk_mul_f16 v154, v48, v34 op_sel:[1,0] op_sel_hi:[1,1]
	v_pk_mul_f16 v155, v48, v35 op_sel:[1,0] op_sel_hi:[1,1]
	v_mfma_f32_32x32x16_f16 a[0:15], v[144:147], v[84:87], a[0:15]
	s_cmp_le_u32 s22, 16
	s_cselect_b32 s41, 0x4000, 0
	s_add_u32 s20, s20, s41
	s_addc_u32 s21, s21, 0
	s_add_u32 s18, s18, 0x4000
	s_cmp_eq_u32 s18, 0x18000
	s_cselect_b32 s18, 0, s18
	v_pk_fma_f16 v152, v40, v36, v152 op_sel:[1,0,0] op_sel_hi:[1,1,1]
	v_pk_fma_f16 v153, v40, v37, v153 op_sel:[1,0,0] op_sel_hi:[1,1,1]
	v_pk_fma_f16 v154, v40, v38, v154 op_sel:[1,0,0] op_sel_hi:[1,1,1]
	v_pk_fma_f16 v155, v40, v39, v155 op_sel:[1,0,0] op_sel_hi:[1,1,1]
	v_mfma_f32_32x32x16_f16 a[16:31], v[148:151], v[88:91], a[16:31]
	v_pk_mul_f16 v156, v48, v36 op_sel:[1,0] op_sel_hi:[1,1]
	v_pk_mul_f16 v157, v48, v37 op_sel:[1,0] op_sel_hi:[1,1]
	v_pk_mul_f16 v158, v48, v38 op_sel:[1,0] op_sel_hi:[1,1]
	v_pk_mul_f16 v159, v48, v39 op_sel:[1,0] op_sel_hi:[1,1]
	v_mfma_f32_32x32x16_f16 a[0:15], v[148:151], v[92:95], a[0:15]
	v_pk_fma_f16 v156, v40, v32, v156 op_sel:[1,0,0] op_sel_hi:[1,1,1] neg_lo:[0,0,1] neg_hi:[0,0,1]
	v_pk_fma_f16 v157, v40, v33, v157 op_sel:[1,0,0] op_sel_hi:[1,1,1] neg_lo:[0,0,1] neg_hi:[0,0,1]
	v_pk_fma_f16 v158, v40, v34, v158 op_sel:[1,0,0] op_sel_hi:[1,1,1] neg_lo:[0,0,1] neg_hi:[0,0,1]
	v_pk_fma_f16 v159, v40, v35, v159 op_sel:[1,0,0] op_sel_hi:[1,1,1] neg_lo:[0,0,1] neg_hi:[0,0,1]
	ds_read_b128 v[112:115], v161 offset:8192
	ds_read_b128 v[116:119], v161 offset:9216
	ds_read_b128 v[120:123], v161 offset:10240
	ds_read_b128 v[124:127], v161 offset:11264
	s_waitcnt lgkmcnt(4)
	v_mfma_f32_32x32x16_f16 a[16:31], v[152:155], v[96:99], a[16:31]
	s_add_u32 s14, s14, 1
	s_cmp_eq_u32 s14, 16
	s_cselect_b32 s42, 1, 0
	s_add_u32 s13, s13, s42
	s_cmp_eq_u32 s42, 1
	s_cselect_b32 s14, s13, s14
	v_pk_mul_f16 v144, v49, v32 op_sel:[0,0] op_sel_hi:[0,1]
	v_pk_mul_f16 v145, v49, v33 op_sel:[0,0] op_sel_hi:[0,1]
	v_pk_mul_f16 v146, v49, v34 op_sel:[0,0] op_sel_hi:[0,1]
	v_pk_mul_f16 v147, v49, v35 op_sel:[0,0] op_sel_hi:[0,1]
	v_mfma_f32_32x32x16_f16 a[0:15], v[152:155], v[100:103], a[0:15]
	s_min_u32 s43, s13, 15
	s_min_u32 s44, s14, 15
	s_lshl_b32 s45, s44, 16
	s_add_u32 s24, s8, s45
	s_addc_u32 s25, s9, 0
	s_add_u32 s26, s24, 0x100000
	s_addc_u32 s27, s25, 0
	s_lshl_b32 s45, s43, 16
	s_add_u32 s28, s8, s45
	s_addc_u32 s29, s9, 0
	s_add_u32 s30, s28, 0x100000
	s_addc_u32 s31, s29, 0
	v_pk_fma_f16 v144, v41, v36, v144 op_sel:[0,0,0] op_sel_hi:[0,1,1]
	v_pk_fma_f16 v145, v41, v37, v145 op_sel:[0,0,0] op_sel_hi:[0,1,1]
	v_pk_fma_f16 v146, v41, v38, v146 op_sel:[0,0,0] op_sel_hi:[0,1,1]
	v_pk_fma_f16 v147, v41, v39, v147 op_sel:[0,0,0] op_sel_hi:[0,1,1]
	v_mfma_f32_32x32x16_f16 a[16:31], v[156:159], v[104:107], a[16:31]
	global_load_dwordx4 v[60:63], v164, s[24:25]
	global_load_dwordx4 v[56:59], v164, s[26:27]
	global_load_dwordx4 v[64:67], v165, s[28:29]
	global_load_dwordx4 v[68:71], v166, s[28:29]
	global_load_dwordx4 v[72:75], v165, s[30:31]
	global_load_dwordx4 v[76:79], v166, s[30:31]
	v_pk_mul_f16 v148, v49, v36 op_sel:[0,0] op_sel_hi:[0,1]
	v_pk_mul_f16 v149, v49, v37 op_sel:[0,0] op_sel_hi:[0,1]
	v_pk_mul_f16 v150, v49, v38 op_sel:[0,0] op_sel_hi:[0,1]
	v_pk_mul_f16 v151, v49, v39 op_sel:[0,0] op_sel_hi:[0,1]
	v_mfma_f32_32x32x16_f16 a[0:15], v[156:159], v[108:111], a[0:15]
	v_pk_fma_f16 v148, v41, v32, v148 op_sel:[0,0,0] op_sel_hi:[0,1,1] neg_lo:[0,0,1] neg_hi:[0,0,1]
	v_pk_fma_f16 v149, v41, v33, v149 op_sel:[0,0,0] op_sel_hi:[0,1,1] neg_lo:[0,0,1] neg_hi:[0,0,1]
	v_pk_fma_f16 v150, v41, v34, v150 op_sel:[0,0,0] op_sel_hi:[0,1,1] neg_lo:[0,0,1] neg_hi:[0,0,1]
	v_pk_fma_f16 v151, v41, v35, v151 op_sel:[0,0,0] op_sel_hi:[0,1,1] neg_lo:[0,0,1] neg_hi:[0,0,1]
	ds_read_b128 v[128:131], v161 offset:12288
	ds_read_b128 v[132:135], v161 offset:13312
	ds_read_b128 v[136:139], v161 offset:14336
	ds_read_b128 v[140:143], v161 offset:15360
	s_add_u32 s19, s19, 0x4000
	s_cmp_eq_u32 s19, 0x18000
	s_cselect_b32 s19, 0, s19
	v_add_u32_e32 v161, s19, v160
	s_waitcnt lgkmcnt(4)
	v_mfma_f32_32x32x16_f16 a[16:31], v[144:147], v[112:115], a[16:31]
	v_pk_mul_f16 v152, v49, v32 op_sel:[1,0] op_sel_hi:[1,1]
	v_pk_mul_f16 v153, v49, v33 op_sel:[1,0] op_sel_hi:[1,1]
	v_pk_mul_f16 v154, v49, v34 op_sel:[1,0] op_sel_hi:[1,1]
	v_pk_mul_f16 v155, v49, v35 op_sel:[1,0] op_sel_hi:[1,1]
	v_mfma_f32_32x32x16_f16 a[0:15], v[144:147], v[116:119], a[0:15]
	v_pk_fma_f16 v152, v41, v36, v152 op_sel:[1,0,0] op_sel_hi:[1,1,1]
	v_pk_fma_f16 v153, v41, v37, v153 op_sel:[1,0,0] op_sel_hi:[1,1,1]
	v_pk_fma_f16 v154, v41, v38, v154 op_sel:[1,0,0] op_sel_hi:[1,1,1]
	v_pk_fma_f16 v155, v41, v39, v155 op_sel:[1,0,0] op_sel_hi:[1,1,1]
	v_mfma_f32_32x32x16_f16 a[16:31], v[148:151], v[120:123], a[16:31]
	v_pk_mul_f16 v156, v49, v36 op_sel:[1,0] op_sel_hi:[1,1]
	v_pk_mul_f16 v157, v49, v37 op_sel:[1,0] op_sel_hi:[1,1]
	v_pk_mul_f16 v158, v49, v38 op_sel:[1,0] op_sel_hi:[1,1]
	v_pk_mul_f16 v159, v49, v39 op_sel:[1,0] op_sel_hi:[1,1]
	v_mfma_f32_32x32x16_f16 a[0:15], v[148:151], v[124:127], a[0:15]
	v_pk_fma_f16 v156, v41, v32, v156 op_sel:[1,0,0] op_sel_hi:[1,1,1] neg_lo:[0,0,1] neg_hi:[0,0,1]
	v_pk_fma_f16 v157, v41, v33, v157 op_sel:[1,0,0] op_sel_hi:[1,1,1] neg_lo:[0,0,1] neg_hi:[0,0,1]
	v_pk_fma_f16 v158, v41, v34, v158 op_sel:[1,0,0] op_sel_hi:[1,1,1] neg_lo:[0,0,1] neg_hi:[0,0,1]
	v_pk_fma_f16 v159, v41, v35, v159 op_sel:[1,0,0] op_sel_hi:[1,1,1] neg_lo:[0,0,1] neg_hi:[0,0,1]
	ds_read_b128 v[80:83], v161
	ds_read_b128 v[84:87], v161 offset:1024
	ds_read_b128 v[88:91], v161 offset:2048
	ds_read_b128 v[92:95], v161 offset:3072
	s_waitcnt lgkmcnt(4)
	v_mfma_f32_32x32x16_f16 a[16:31], v[152:155], v[128:131], a[16:31]
	v_pk_mul_f16 v144, v50, v32 op_sel:[0,0] op_sel_hi:[0,1]
	v_pk_mul_f16 v145, v50, v33 op_sel:[0,0] op_sel_hi:[0,1]
	v_pk_mul_f16 v146, v50, v34 op_sel:[0,0] op_sel_hi:[0,1]
	v_pk_mul_f16 v147, v50, v35 op_sel:[0,0] op_sel_hi:[0,1]
	v_mfma_f32_32x32x16_f16 a[0:15], v[152:155], v[132:135], a[0:15]
	v_pk_fma_f16 v144, v42, v36, v144 op_sel:[0,0,0] op_sel_hi:[0,1,1]
	v_pk_fma_f16 v145, v42, v37, v145 op_sel:[0,0,0] op_sel_hi:[0,1,1]
	v_pk_fma_f16 v146, v42, v38, v146 op_sel:[0,0,0] op_sel_hi:[0,1,1]
	v_pk_fma_f16 v147, v42, v39, v147 op_sel:[0,0,0] op_sel_hi:[0,1,1]
	v_mfma_f32_32x32x16_f16 a[16:31], v[156:159], v[136:139], a[16:31]
	v_pk_mul_f16 v148, v50, v36 op_sel:[0,0] op_sel_hi:[0,1]
	v_pk_mul_f16 v149, v50, v37 op_sel:[0,0] op_sel_hi:[0,1]
	v_pk_mul_f16 v150, v50, v38 op_sel:[0,0] op_sel_hi:[0,1]
	v_pk_mul_f16 v151, v50, v39 op_sel:[0,0] op_sel_hi:[0,1]
	v_mfma_f32_32x32x16_f16 a[0:15], v[156:159], v[140:143], a[0:15]
	v_pk_fma_f16 v148, v42, v32, v148 op_sel:[0,0,0] op_sel_hi:[0,1,1] neg_lo:[0,0,1] neg_hi:[0,0,1]
	v_pk_fma_f16 v149, v42, v33, v149 op_sel:[0,0,0] op_sel_hi:[0,1,1] neg_lo:[0,0,1] neg_hi:[0,0,1]
	v_pk_fma_f16 v150, v42, v34, v150 op_sel:[0,0,0] op_sel_hi:[0,1,1] neg_lo:[0,0,1] neg_hi:[0,0,1]
	v_pk_fma_f16 v151, v42, v35, v151 op_sel:[0,0,0] op_sel_hi:[0,1,1] neg_lo:[0,0,1] neg_hi:[0,0,1]
	ds_read_b128 v[96:99], v161 offset:4096
	ds_read_b128 v[100:103], v161 offset:5120
	ds_read_b128 v[104:107], v161 offset:6144
	ds_read_b128 v[108:111], v161 offset:7168
	s_add_u32 s17, s17, 1
	s_cmp_eq_u32 s17, 17
	s_cbranch_scc1 .Lk2_epi

.Lk2_b01:
	s_waitcnt lgkmcnt(4)
	v_mfma_f32_32x32x16_f16 a[16:31], v[144:147], v[80:83], a[16:31]
	s_cmp_le_u32 s22, 16
	s_cselect_b32 s40, s18, 0x18000
	s_add_u32 m0, s40, s35
	s_add_u32 s22, s22, 1
	global_load_lds_dwordx4 v168, s[20:21]
	global_load_lds_dwordx4 v168, s[20:21] offset:1024
	v_pk_mul_f16 v152, v50, v32 op_sel:[1,0] op_sel_hi:[1,1]
	v_pk_mul_f16 v153, v50, v33 op_sel:[1,0] op_sel_hi:[1,1]
	v_pk_mul_f16 v154, v50, v34 op_sel:[1,0] op_sel_hi:[1,1]
	v_pk_mul_f16 v155, v50, v35 op_sel:[1,0] op_sel_hi:[1,1]
	v_mfma_f32_32x32x16_f16 a[0:15], v[144:147], v[84:87], a[0:15]
	s_cmp_le_u32 s22, 16
	s_cselect_b32 s41, 0x4000, 0
	s_add_u32 s20, s20, s41
	s_addc_u32 s21, s21, 0
	s_add_u32 s18, s18, 0x4000
	s_cmp_eq_u32 s18, 0x18000
	s_cselect_b32 s18, 0, s18
	v_pk_fma_f16 v152, v42, v36, v152 op_sel:[1,0,0] op_sel_hi:[1,1,1]
	v_pk_fma_f16 v153, v42, v37, v153 op_sel:[1,0,0] op_sel_hi:[1,1,1]
	v_pk_fma_f16 v154, v42, v38, v154 op_sel:[1,0,0] op_sel_hi:[1,1,1]
	v_pk_fma_f16 v155, v42, v39, v155 op_sel:[1,0,0] op_sel_hi:[1,1,1]
	v_mfma_f32_32x32x16_f16 a[16:31], v[148:151], v[88:91], a[16:31]
	v_pk_mul_f16 v156, v50, v36 op_sel:[1,0] op_sel_hi:[1,1]
	v_pk_mul_f16 v157, v50, v37 op_sel:[1,0] op_sel_hi:[1,1]
	v_pk_mul_f16 v158, v50, v38 op_sel:[1,0] op_sel_hi:[1,1]
	v_pk_mul_f16 v159, v50, v39 op_sel:[1,0] op_sel_hi:[1,1]
	v_mfma_f32_32x32x16_f16 a[0:15], v[148:151], v[92:95], a[0:15]
	v_pk_fma_f16 v156, v42, v32, v156 op_sel:[1,0,0] op_sel_hi:[1,1,1] neg_lo:[0,0,1] neg_hi:[0,0,1]
	v_pk_fma_f16 v157, v42, v33, v157 op_sel:[1,0,0] op_sel_hi:[1,1,1] neg_lo:[0,0,1] neg_hi:[0,0,1]
	v_pk_fma_f16 v158, v42, v34, v158 op_sel:[1,0,0] op_sel_hi:[1,1,1] neg_lo:[0,0,1] neg_hi:[0,0,1]
	v_pk_fma_f16 v159, v42, v35, v159 op_sel:[1,0,0] op_sel_hi:[1,1,1] neg_lo:[0,0,1] neg_hi:[0,0,1]
	ds_read_b128 v[112:115], v161 offset:8192
	ds_read_b128 v[116:119], v161 offset:9216
	ds_read_b128 v[120:123], v161 offset:10240
	ds_read_b128 v[124:127], v161 offset:11264
	s_waitcnt lgkmcnt(4)
	v_mfma_f32_32x32x16_f16 a[16:31], v[152:155], v[96:99], a[16:31]
	v_pk_mul_f16 v144, v51, v32 op_sel:[0,0] op_sel_hi:[0,1]
	v_pk_mul_f16 v145, v51, v33 op_sel:[0,0] op_sel_hi:[0,1]
	v_pk_mul_f16 v146, v51, v34 op_sel:[0,0] op_sel_hi:[0,1]
	v_pk_mul_f16 v147, v51, v35 op_sel:[0,0] op_sel_hi:[0,1]
	v_mfma_f32_32x32x16_f16 a[0:15], v[152:155], v[100:103], a[0:15]
	v_pk_fma_f16 v144, v43, v36, v144 op_sel:[0,0,0] op_sel_hi:[0,1,1]
	v_pk_fma_f16 v145, v43, v37, v145 op_sel:[0,0,0] op_sel_hi:[0,1,1]
	v_pk_fma_f16 v146, v43, v38, v146 op_sel:[0,0,0] op_sel_hi:[0,1,1]
	v_pk_fma_f16 v147, v43, v39, v147 op_sel:[0,0,0] op_sel_hi:[0,1,1]
	v_mfma_f32_32x32x16_f16 a[16:31], v[156:159], v[104:107], a[16:31]
	v_pk_mul_f16 v148, v51, v36 op_sel:[0,0] op_sel_hi:[0,1]
	v_pk_mul_f16 v149, v51, v37 op_sel:[0,0] op_sel_hi:[0,1]
	v_pk_mul_f16 v150, v51, v38 op_sel:[0,0] op_sel_hi:[0,1]
	v_pk_mul_f16 v151, v51, v39 op_sel:[0,0] op_sel_hi:[0,1]
	v_mfma_f32_32x32x16_f16 a[0:15], v[156:159], v[108:111], a[0:15]
	v_pk_fma_f16 v148, v43, v32, v148 op_sel:[0,0,0] op_sel_hi:[0,1,1] neg_lo:[0,0,1] neg_hi:[0,0,1]
	v_pk_fma_f16 v149, v43, v33, v149 op_sel:[0,0,0] op_sel_hi:[0,1,1] neg_lo:[0,0,1] neg_hi:[0,0,1]
	v_pk_fma_f16 v150, v43, v34, v150 op_sel:[0,0,0] op_sel_hi:[0,1,1] neg_lo:[0,0,1] neg_hi:[0,0,1]
	v_pk_fma_f16 v151, v43, v35, v151 op_sel:[0,0,0] op_sel_hi:[0,1,1] neg_lo:[0,0,1] neg_hi:[0,0,1]
	ds_read_b128 v[128:131], v161 offset:12288
	ds_read_b128 v[132:135], v161 offset:13312
	ds_read_b128 v[136:139], v161 offset:14336
	ds_read_b128 v[140:143], v161 offset:15360
	s_add_u32 s19, s19, 0x4000
	s_cmp_eq_u32 s19, 0x18000
	s_cselect_b32 s19, 0, s19
	v_add_u32_e32 v161, s19, v160
	s_waitcnt lgkmcnt(4)
	v_mfma_f32_32x32x16_f16 a[16:31], v[144:147], v[112:115], a[16:31]
	v_pk_mul_f16 v152, v51, v32 op_sel:[1,0] op_sel_hi:[1,1]
	v_pk_mul_f16 v153, v51, v33 op_sel:[1,0] op_sel_hi:[1,1]
	v_pk_mul_f16 v154, v51, v34 op_sel:[1,0] op_sel_hi:[1,1]
	v_pk_mul_f16 v155, v51, v35 op_sel:[1,0] op_sel_hi:[1,1]
	v_mfma_f32_32x32x16_f16 a[0:15], v[144:147], v[116:119], a[0:15]
	v_pk_fma_f16 v152, v43, v36, v152 op_sel:[1,0,0] op_sel_hi:[1,1,1]
	v_pk_fma_f16 v153, v43, v37, v153 op_sel:[1,0,0] op_sel_hi:[1,1,1]
	v_pk_fma_f16 v154, v43, v38, v154 op_sel:[1,0,0] op_sel_hi:[1,1,1]
	v_pk_fma_f16 v155, v43, v39, v155 op_sel:[1,0,0] op_sel_hi:[1,1,1]
	v_mfma_f32_32x32x16_f16 a[16:31], v[148:151], v[120:123], a[16:31]
	v_pk_mul_f16 v156, v51, v36 op_sel:[1,0] op_sel_hi:[1,1]
	v_pk_mul_f16 v157, v51, v37 op_sel:[1,0] op_sel_hi:[1,1]
	v_pk_mul_f16 v158, v51, v38 op_sel:[1,0] op_sel_hi:[1,1]
	v_pk_mul_f16 v159, v51, v39 op_sel:[1,0] op_sel_hi:[1,1]
	v_mfma_f32_32x32x16_f16 a[0:15], v[148:151], v[124:127], a[0:15]
	v_pk_fma_f16 v156, v43, v32, v156 op_sel:[1,0,0] op_sel_hi:[1,1,1] neg_lo:[0,0,1] neg_hi:[0,0,1]
	v_pk_fma_f16 v157, v43, v33, v157 op_sel:[1,0,0] op_sel_hi:[1,1,1] neg_lo:[0,0,1] neg_hi:[0,0,1]
	v_pk_fma_f16 v158, v43, v34, v158 op_sel:[1,0,0] op_sel_hi:[1,1,1] neg_lo:[0,0,1] neg_hi:[0,0,1]
	v_pk_fma_f16 v159, v43, v35, v159 op_sel:[1,0,0] op_sel_hi:[1,1,1] neg_lo:[0,0,1] neg_hi:[0,0,1]
	ds_read_b128 v[80:83], v161
	ds_read_b128 v[84:87], v161 offset:1024
	ds_read_b128 v[88:91], v161 offset:2048
	ds_read_b128 v[92:95], v161 offset:3072
	s_waitcnt lgkmcnt(4)
	v_mfma_f32_32x32x16_f16 a[16:31], v[152:155], v[128:131], a[16:31]
	v_pk_mul_f16 v144, v52, v32 op_sel:[0,0] op_sel_hi:[0,1]
	v_pk_mul_f16 v145, v52, v33 op_sel:[0,0] op_sel_hi:[0,1]
	v_pk_mul_f16 v146, v52, v34 op_sel:[0,0] op_sel_hi:[0,1]
	v_pk_mul_f16 v147, v52, v35 op_sel:[0,0] op_sel_hi:[0,1]
	v_mfma_f32_32x32x16_f16 a[0:15], v[152:155], v[132:135], a[0:15]
	v_pk_fma_f16 v144, v44, v36, v144 op_sel:[0,0,0] op_sel_hi:[0,1,1]
	v_pk_fma_f16 v145, v44, v37, v145 op_sel:[0,0,0] op_sel_hi:[0,1,1]
	v_pk_fma_f16 v146, v44, v38, v146 op_sel:[0,0,0] op_sel_hi:[0,1,1]
	v_pk_fma_f16 v147, v44, v39, v147 op_sel:[0,0,0] op_sel_hi:[0,1,1]
	v_mfma_f32_32x32x16_f16 a[16:31], v[156:159], v[136:139], a[16:31]
	v_pk_mul_f16 v148, v52, v36 op_sel:[0,0] op_sel_hi:[0,1]
	v_pk_mul_f16 v149, v52, v37 op_sel:[0,0] op_sel_hi:[0,1]
	v_pk_mul_f16 v150, v52, v38 op_sel:[0,0] op_sel_hi:[0,1]
	v_pk_mul_f16 v151, v52, v39 op_sel:[0,0] op_sel_hi:[0,1]
	v_mfma_f32_32x32x16_f16 a[0:15], v[156:159], v[140:143], a[0:15]
	v_pk_fma_f16 v148, v44, v32, v148 op_sel:[0,0,0] op_sel_hi:[0,1,1] neg_lo:[0,0,1] neg_hi:[0,0,1]
	v_pk_fma_f16 v149, v44, v33, v149 op_sel:[0,0,0] op_sel_hi:[0,1,1] neg_lo:[0,0,1] neg_hi:[0,0,1]
	v_pk_fma_f16 v150, v44, v34, v150 op_sel:[0,0,0] op_sel_hi:[0,1,1] neg_lo:[0,0,1] neg_hi:[0,0,1]
	v_pk_fma_f16 v151, v44, v35, v151 op_sel:[0,0,0] op_sel_hi:[0,1,1] neg_lo:[0,0,1] neg_hi:[0,0,1]
	ds_read_b128 v[96:99], v161 offset:4096
	ds_read_b128 v[100:103], v161 offset:5120
	ds_read_b128 v[104:107], v161 offset:6144
	ds_read_b128 v[108:111], v161 offset:7168
	s_add_u32 s17, s17, 1
	s_cmp_eq_u32 s17, 17
	s_cbranch_scc1 .Lk2_epi

.Lk2_b02:
	s_waitcnt lgkmcnt(4)
	v_mfma_f32_32x32x16_f16 a[16:31], v[144:147], v[80:83], a[16:31]
	s_cmp_le_u32 s22, 16
	s_cselect_b32 s40, s18, 0x18000
	s_add_u32 m0, s40, s35
	s_add_u32 s22, s22, 1
	global_load_lds_dwordx4 v168, s[20:21]
	global_load_lds_dwordx4 v168, s[20:21] offset:1024
	v_pk_mul_f16 v152, v52, v32 op_sel:[1,0] op_sel_hi:[1,1]
	v_pk_mul_f16 v153, v52, v33 op_sel:[1,0] op_sel_hi:[1,1]
	v_pk_mul_f16 v154, v52, v34 op_sel:[1,0] op_sel_hi:[1,1]
	v_pk_mul_f16 v155, v52, v35 op_sel:[1,0] op_sel_hi:[1,1]
	v_mfma_f32_32x32x16_f16 a[0:15], v[144:147], v[84:87], a[0:15]
	s_cmp_le_u32 s22, 16
	s_cselect_b32 s41, 0x4000, 0
	s_add_u32 s20, s20, s41
	s_addc_u32 s21, s21, 0
	s_add_u32 s18, s18, 0x4000
	s_cmp_eq_u32 s18, 0x18000
	s_cselect_b32 s18, 0, s18
	v_pk_fma_f16 v152, v44, v36, v152 op_sel:[1,0,0] op_sel_hi:[1,1,1]
	v_pk_fma_f16 v153, v44, v37, v153 op_sel:[1,0,0] op_sel_hi:[1,1,1]
	v_pk_fma_f16 v154, v44, v38, v154 op_sel:[1,0,0] op_sel_hi:[1,1,1]
	v_pk_fma_f16 v155, v44, v39, v155 op_sel:[1,0,0] op_sel_hi:[1,1,1]
	v_mfma_f32_32x32x16_f16 a[16:31], v[148:151], v[88:91], a[16:31]
	v_pk_mul_f16 v156, v52, v36 op_sel:[1,0] op_sel_hi:[1,1]
	v_pk_mul_f16 v157, v52, v37 op_sel:[1,0] op_sel_hi:[1,1]
	v_pk_mul_f16 v158, v52, v38 op_sel:[1,0] op_sel_hi:[1,1]
	v_pk_mul_f16 v159, v52, v39 op_sel:[1,0] op_sel_hi:[1,1]
	v_mfma_f32_32x32x16_f16 a[0:15], v[148:151], v[92:95], a[0:15]
	v_pk_fma_f16 v156, v44, v32, v156 op_sel:[1,0,0] op_sel_hi:[1,1,1] neg_lo:[0,0,1] neg_hi:[0,0,1]
	v_pk_fma_f16 v157, v44, v33, v157 op_sel:[1,0,0] op_sel_hi:[1,1,1] neg_lo:[0,0,1] neg_hi:[0,0,1]
	v_pk_fma_f16 v158, v44, v34, v158 op_sel:[1,0,0] op_sel_hi:[1,1,1] neg_lo:[0,0,1] neg_hi:[0,0,1]
	v_pk_fma_f16 v159, v44, v35, v159 op_sel:[1,0,0] op_sel_hi:[1,1,1] neg_lo:[0,0,1] neg_hi:[0,0,1]
	ds_read_b128 v[112:115], v161 offset:8192
	ds_read_b128 v[116:119], v161 offset:9216
	ds_read_b128 v[120:123], v161 offset:10240
	ds_read_b128 v[124:127], v161 offset:11264
	s_waitcnt lgkmcnt(4)
	v_mfma_f32_32x32x16_f16 a[16:31], v[152:155], v[96:99], a[16:31]
	v_pk_mul_f16 v144, v53, v32 op_sel:[0,0] op_sel_hi:[0,1]
	v_pk_mul_f16 v145, v53, v33 op_sel:[0,0] op_sel_hi:[0,1]
	v_pk_mul_f16 v146, v53, v34 op_sel:[0,0] op_sel_hi:[0,1]
	v_pk_mul_f16 v147, v53, v35 op_sel:[0,0] op_sel_hi:[0,1]
	v_mfma_f32_32x32x16_f16 a[0:15], v[152:155], v[100:103], a[0:15]
	v_pk_fma_f16 v144, v45, v36, v144 op_sel:[0,0,0] op_sel_hi:[0,1,1]
	v_pk_fma_f16 v145, v45, v37, v145 op_sel:[0,0,0] op_sel_hi:[0,1,1]
	v_pk_fma_f16 v146, v45, v38, v146 op_sel:[0,0,0] op_sel_hi:[0,1,1]
	v_pk_fma_f16 v147, v45, v39, v147 op_sel:[0,0,0] op_sel_hi:[0,1,1]
	v_mfma_f32_32x32x16_f16 a[16:31], v[156:159], v[104:107], a[16:31]
	v_pk_mul_f16 v148, v53, v36 op_sel:[0,0] op_sel_hi:[0,1]
	v_pk_mul_f16 v149, v53, v37 op_sel:[0,0] op_sel_hi:[0,1]
	v_pk_mul_f16 v150, v53, v38 op_sel:[0,0] op_sel_hi:[0,1]
	v_pk_mul_f16 v151, v53, v39 op_sel:[0,0] op_sel_hi:[0,1]
	v_mfma_f32_32x32x16_f16 a[0:15], v[156:159], v[108:111], a[0:15]
	v_pk_fma_f16 v148, v45, v32, v148 op_sel:[0,0,0] op_sel_hi:[0,1,1] neg_lo:[0,0,1] neg_hi:[0,0,1]
	v_pk_fma_f16 v149, v45, v33, v149 op_sel:[0,0,0] op_sel_hi:[0,1,1] neg_lo:[0,0,1] neg_hi:[0,0,1]
	v_pk_fma_f16 v150, v45, v34, v150 op_sel:[0,0,0] op_sel_hi:[0,1,1] neg_lo:[0,0,1] neg_hi:[0,0,1]
	v_pk_fma_f16 v151, v45, v35, v151 op_sel:[0,0,0] op_sel_hi:[0,1,1] neg_lo:[0,0,1] neg_hi:[0,0,1]
	ds_read_b128 v[128:131], v161 offset:12288
	ds_read_b128 v[132:135], v161 offset:13312
	ds_read_b128 v[136:139], v161 offset:14336
	ds_read_b128 v[140:143], v161 offset:15360
	s_add_u32 s19, s19, 0x4000
	s_cmp_eq_u32 s19, 0x18000
	s_cselect_b32 s19, 0, s19
	v_add_u32_e32 v161, s19, v160
	s_waitcnt lgkmcnt(4)
	v_mfma_f32_32x32x16_f16 a[16:31], v[144:147], v[112:115], a[16:31]
	v_pk_mul_f16 v152, v53, v32 op_sel:[1,0] op_sel_hi:[1,1]
	v_pk_mul_f16 v153, v53, v33 op_sel:[1,0] op_sel_hi:[1,1]
	v_pk_mul_f16 v154, v53, v34 op_sel:[1,0] op_sel_hi:[1,1]
	v_pk_mul_f16 v155, v53, v35 op_sel:[1,0] op_sel_hi:[1,1]
	v_mfma_f32_32x32x16_f16 a[0:15], v[144:147], v[116:119], a[0:15]
	v_pk_fma_f16 v152, v45, v36, v152 op_sel:[1,0,0] op_sel_hi:[1,1,1]
	v_pk_fma_f16 v153, v45, v37, v153 op_sel:[1,0,0] op_sel_hi:[1,1,1]
	v_pk_fma_f16 v154, v45, v38, v154 op_sel:[1,0,0] op_sel_hi:[1,1,1]
	v_pk_fma_f16 v155, v45, v39, v155 op_sel:[1,0,0] op_sel_hi:[1,1,1]
	v_mfma_f32_32x32x16_f16 a[16:31], v[148:151], v[120:123], a[16:31]
	v_pk_mul_f16 v156, v53, v36 op_sel:[1,0] op_sel_hi:[1,1]
	v_pk_mul_f16 v157, v53, v37 op_sel:[1,0] op_sel_hi:[1,1]
	v_pk_mul_f16 v158, v53, v38 op_sel:[1,0] op_sel_hi:[1,1]
	v_pk_mul_f16 v159, v53, v39 op_sel:[1,0] op_sel_hi:[1,1]
	v_mfma_f32_32x32x16_f16 a[0:15], v[148:151], v[124:127], a[0:15]
	v_pk_fma_f16 v156, v45, v32, v156 op_sel:[1,0,0] op_sel_hi:[1,1,1] neg_lo:[0,0,1] neg_hi:[0,0,1]
	v_pk_fma_f16 v157, v45, v33, v157 op_sel:[1,0,0] op_sel_hi:[1,1,1] neg_lo:[0,0,1] neg_hi:[0,0,1]
	v_pk_fma_f16 v158, v45, v34, v158 op_sel:[1,0,0] op_sel_hi:[1,1,1] neg_lo:[0,0,1] neg_hi:[0,0,1]
	v_pk_fma_f16 v159, v45, v35, v159 op_sel:[1,0,0] op_sel_hi:[1,1,1] neg_lo:[0,0,1] neg_hi:[0,0,1]
	ds_read_b128 v[80:83], v161
	ds_read_b128 v[84:87], v161 offset:1024
	ds_read_b128 v[88:91], v161 offset:2048
	ds_read_b128 v[92:95], v161 offset:3072
	s_waitcnt lgkmcnt(4)
	v_mfma_f32_32x32x16_f16 a[16:31], v[152:155], v[128:131], a[16:31]
	v_pk_mul_f16 v144, v54, v32 op_sel:[0,0] op_sel_hi:[0,1]
	v_pk_mul_f16 v145, v54, v33 op_sel:[0,0] op_sel_hi:[0,1]
	v_pk_mul_f16 v146, v54, v34 op_sel:[0,0] op_sel_hi:[0,1]
	v_pk_mul_f16 v147, v54, v35 op_sel:[0,0] op_sel_hi:[0,1]
	v_mfma_f32_32x32x16_f16 a[0:15], v[152:155], v[132:135], a[0:15]
	v_pk_fma_f16 v144, v46, v36, v144 op_sel:[0,0,0] op_sel_hi:[0,1,1]
	v_pk_fma_f16 v145, v46, v37, v145 op_sel:[0,0,0] op_sel_hi:[0,1,1]
	v_pk_fma_f16 v146, v46, v38, v146 op_sel:[0,0,0] op_sel_hi:[0,1,1]
	v_pk_fma_f16 v147, v46, v39, v147 op_sel:[0,0,0] op_sel_hi:[0,1,1]
	v_mfma_f32_32x32x16_f16 a[16:31], v[156:159], v[136:139], a[16:31]
	v_pk_mul_f16 v148, v54, v36 op_sel:[0,0] op_sel_hi:[0,1]
	v_pk_mul_f16 v149, v54, v37 op_sel:[0,0] op_sel_hi:[0,1]
	v_pk_mul_f16 v150, v54, v38 op_sel:[0,0] op_sel_hi:[0,1]
	v_pk_mul_f16 v151, v54, v39 op_sel:[0,0] op_sel_hi:[0,1]
	v_mfma_f32_32x32x16_f16 a[0:15], v[156:159], v[140:143], a[0:15]
	v_pk_fma_f16 v148, v46, v32, v148 op_sel:[0,0,0] op_sel_hi:[0,1,1] neg_lo:[0,0,1] neg_hi:[0,0,1]
	v_pk_fma_f16 v149, v46, v33, v149 op_sel:[0,0,0] op_sel_hi:[0,1,1] neg_lo:[0,0,1] neg_hi:[0,0,1]
	v_pk_fma_f16 v150, v46, v34, v150 op_sel:[0,0,0] op_sel_hi:[0,1,1] neg_lo:[0,0,1] neg_hi:[0,0,1]
	v_pk_fma_f16 v151, v46, v35, v151 op_sel:[0,0,0] op_sel_hi:[0,1,1] neg_lo:[0,0,1] neg_hi:[0,0,1]
	ds_read_b128 v[96:99], v161 offset:4096
	ds_read_b128 v[100:103], v161 offset:5120
	ds_read_b128 v[104:107], v161 offset:6144
	ds_read_b128 v[108:111], v161 offset:7168
	s_add_u32 s17, s17, 1
	s_cmp_eq_u32 s17, 17
	s_cbranch_scc1 .Lk2_epi

.Lk2_b03:
	s_waitcnt lgkmcnt(4)
	v_mfma_f32_32x32x16_f16 a[16:31], v[144:147], v[80:83], a[16:31]
	s_cmp_le_u32 s22, 16
	s_cselect_b32 s40, s18, 0x18000
	s_add_u32 m0, s40, s35
	s_add_u32 s22, s22, 1
	global_load_lds_dwordx4 v168, s[20:21]
	global_load_lds_dwordx4 v168, s[20:21] offset:1024
	v_pk_mul_f16 v152, v54, v32 op_sel:[1,0] op_sel_hi:[1,1]
	v_pk_mul_f16 v153, v54, v33 op_sel:[1,0] op_sel_hi:[1,1]
	v_pk_mul_f16 v154, v54, v34 op_sel:[1,0] op_sel_hi:[1,1]
	v_pk_mul_f16 v155, v54, v35 op_sel:[1,0] op_sel_hi:[1,1]
	v_mfma_f32_32x32x16_f16 a[0:15], v[144:147], v[84:87], a[0:15]
	s_cmp_le_u32 s22, 16
	s_cselect_b32 s41, 0x4000, 0
	s_add_u32 s20, s20, s41
	s_addc_u32 s21, s21, 0
	s_add_u32 s18, s18, 0x4000
	s_cmp_eq_u32 s18, 0x18000
	s_cselect_b32 s18, 0, s18
	v_pk_fma_f16 v152, v46, v36, v152 op_sel:[1,0,0] op_sel_hi:[1,1,1]
	v_pk_fma_f16 v153, v46, v37, v153 op_sel:[1,0,0] op_sel_hi:[1,1,1]
	v_pk_fma_f16 v154, v46, v38, v154 op_sel:[1,0,0] op_sel_hi:[1,1,1]
	v_pk_fma_f16 v155, v46, v39, v155 op_sel:[1,0,0] op_sel_hi:[1,1,1]
	v_mfma_f32_32x32x16_f16 a[16:31], v[148:151], v[88:91], a[16:31]
	v_pk_mul_f16 v156, v54, v36 op_sel:[1,0] op_sel_hi:[1,1]
	v_pk_mul_f16 v157, v54, v37 op_sel:[1,0] op_sel_hi:[1,1]
	v_pk_mul_f16 v158, v54, v38 op_sel:[1,0] op_sel_hi:[1,1]
	v_pk_mul_f16 v159, v54, v39 op_sel:[1,0] op_sel_hi:[1,1]
	v_mfma_f32_32x32x16_f16 a[0:15], v[148:151], v[92:95], a[0:15]
	v_pk_fma_f16 v156, v46, v32, v156 op_sel:[1,0,0] op_sel_hi:[1,1,1] neg_lo:[0,0,1] neg_hi:[0,0,1]
	v_pk_fma_f16 v157, v46, v33, v157 op_sel:[1,0,0] op_sel_hi:[1,1,1] neg_lo:[0,0,1] neg_hi:[0,0,1]
	v_pk_fma_f16 v158, v46, v34, v158 op_sel:[1,0,0] op_sel_hi:[1,1,1] neg_lo:[0,0,1] neg_hi:[0,0,1]
	v_pk_fma_f16 v159, v46, v35, v159 op_sel:[1,0,0] op_sel_hi:[1,1,1] neg_lo:[0,0,1] neg_hi:[0,0,1]
	ds_read_b128 v[112:115], v161 offset:8192
	ds_read_b128 v[116:119], v161 offset:9216
	ds_read_b128 v[120:123], v161 offset:10240
	ds_read_b128 v[124:127], v161 offset:11264
	s_waitcnt lgkmcnt(4)
	v_mfma_f32_32x32x16_f16 a[16:31], v[152:155], v[96:99], a[16:31]
	v_pk_mul_f16 v144, v55, v32 op_sel:[0,0] op_sel_hi:[0,1]
	v_pk_mul_f16 v145, v55, v33 op_sel:[0,0] op_sel_hi:[0,1]
	v_pk_mul_f16 v146, v55, v34 op_sel:[0,0] op_sel_hi:[0,1]
	v_pk_mul_f16 v147, v55, v35 op_sel:[0,0] op_sel_hi:[0,1]
	v_mfma_f32_32x32x16_f16 a[0:15], v[152:155], v[100:103], a[0:15]
	v_pk_fma_f16 v144, v47, v36, v144 op_sel:[0,0,0] op_sel_hi:[0,1,1]
	v_pk_fma_f16 v145, v47, v37, v145 op_sel:[0,0,0] op_sel_hi:[0,1,1]
	v_pk_fma_f16 v146, v47, v38, v146 op_sel:[0,0,0] op_sel_hi:[0,1,1]
	v_pk_fma_f16 v147, v47, v39, v147 op_sel:[0,0,0] op_sel_hi:[0,1,1]
	v_mfma_f32_32x32x16_f16 a[16:31], v[156:159], v[104:107], a[16:31]
	v_pk_mul_f16 v148, v55, v36 op_sel:[0,0] op_sel_hi:[0,1]
	v_pk_mul_f16 v149, v55, v37 op_sel:[0,0] op_sel_hi:[0,1]
	v_pk_mul_f16 v150, v55, v38 op_sel:[0,0] op_sel_hi:[0,1]
	v_pk_mul_f16 v151, v55, v39 op_sel:[0,0] op_sel_hi:[0,1]
	v_mfma_f32_32x32x16_f16 a[0:15], v[156:159], v[108:111], a[0:15]
	v_pk_fma_f16 v148, v47, v32, v148 op_sel:[0,0,0] op_sel_hi:[0,1,1] neg_lo:[0,0,1] neg_hi:[0,0,1]
	v_pk_fma_f16 v149, v47, v33, v149 op_sel:[0,0,0] op_sel_hi:[0,1,1] neg_lo:[0,0,1] neg_hi:[0,0,1]
	v_pk_fma_f16 v150, v47, v34, v150 op_sel:[0,0,0] op_sel_hi:[0,1,1] neg_lo:[0,0,1] neg_hi:[0,0,1]
	v_pk_fma_f16 v151, v47, v35, v151 op_sel:[0,0,0] op_sel_hi:[0,1,1] neg_lo:[0,0,1] neg_hi:[0,0,1]
	ds_read_b128 v[128:131], v161 offset:12288
	ds_read_b128 v[132:135], v161 offset:13312
	ds_read_b128 v[136:139], v161 offset:14336
	ds_read_b128 v[140:143], v161 offset:15360
	s_add_u32 s19, s19, 0x4000
	s_cmp_eq_u32 s19, 0x18000
	s_cselect_b32 s19, 0, s19
	v_add_u32_e32 v161, s19, v160
	s_waitcnt lgkmcnt(4)
	v_mfma_f32_32x32x16_f16 a[16:31], v[144:147], v[112:115], a[16:31]
	v_pk_mul_f16 v152, v55, v32 op_sel:[1,0] op_sel_hi:[1,1]
	v_pk_mul_f16 v153, v55, v33 op_sel:[1,0] op_sel_hi:[1,1]
	v_pk_mul_f16 v154, v55, v34 op_sel:[1,0] op_sel_hi:[1,1]
	v_pk_mul_f16 v155, v55, v35 op_sel:[1,0] op_sel_hi:[1,1]
	v_mfma_f32_32x32x16_f16 a[0:15], v[144:147], v[116:119], a[0:15]
	v_pk_fma_f16 v152, v47, v36, v152 op_sel:[1,0,0] op_sel_hi:[1,1,1]
	v_pk_fma_f16 v153, v47, v37, v153 op_sel:[1,0,0] op_sel_hi:[1,1,1]
	v_pk_fma_f16 v154, v47, v38, v154 op_sel:[1,0,0] op_sel_hi:[1,1,1]
	v_pk_fma_f16 v155, v47, v39, v155 op_sel:[1,0,0] op_sel_hi:[1,1,1]
	v_mfma_f32_32x32x16_f16 a[16:31], v[148:151], v[120:123], a[16:31]
	v_pk_mul_f16 v156, v55, v36 op_sel:[1,0] op_sel_hi:[1,1]
	v_pk_mul_f16 v157, v55, v37 op_sel:[1,0] op_sel_hi:[1,1]
	v_pk_mul_f16 v158, v55, v38 op_sel:[1,0] op_sel_hi:[1,1]
	v_pk_mul_f16 v159, v55, v39 op_sel:[1,0] op_sel_hi:[1,1]
	v_mfma_f32_32x32x16_f16 a[0:15], v[148:151], v[124:127], a[0:15]
	v_pk_fma_f16 v156, v47, v32, v156 op_sel:[1,0,0] op_sel_hi:[1,1,1] neg_lo:[0,0,1] neg_hi:[0,0,1]
	v_pk_fma_f16 v157, v47, v33, v157 op_sel:[1,0,0] op_sel_hi:[1,1,1] neg_lo:[0,0,1] neg_hi:[0,0,1]
	v_pk_fma_f16 v158, v47, v34, v158 op_sel:[1,0,0] op_sel_hi:[1,1,1] neg_lo:[0,0,1] neg_hi:[0,0,1]
	v_pk_fma_f16 v159, v47, v35, v159 op_sel:[1,0,0] op_sel_hi:[1,1,1] neg_lo:[0,0,1] neg_hi:[0,0,1]
	ds_read_b128 v[80:83], v161
	ds_read_b128 v[84:87], v161 offset:1024
	ds_read_b128 v[88:91], v161 offset:2048
	ds_read_b128 v[92:95], v161 offset:3072
	s_waitcnt lgkmcnt(4)
	v_mfma_f32_32x32x16_f16 a[16:31], v[152:155], v[128:131], a[16:31]
	s_waitcnt vmcnt(6)
	v_pk_mul_f16 v144, v72, v56 op_sel:[0,0] op_sel_hi:[0,1]
	v_pk_mul_f16 v145, v72, v57 op_sel:[0,0] op_sel_hi:[0,1]
	v_pk_mul_f16 v146, v72, v58 op_sel:[0,0] op_sel_hi:[0,1]
	v_pk_mul_f16 v147, v72, v59 op_sel:[0,0] op_sel_hi:[0,1]
	v_mfma_f32_32x32x16_f16 a[0:15], v[152:155], v[132:135], a[0:15]
	v_pk_fma_f16 v144, v64, v60, v144 op_sel:[0,0,0] op_sel_hi:[0,1,1]
	v_pk_fma_f16 v145, v64, v61, v145 op_sel:[0,0,0] op_sel_hi:[0,1,1]
	v_pk_fma_f16 v146, v64, v62, v146 op_sel:[0,0,0] op_sel_hi:[0,1,1]
	v_pk_fma_f16 v147, v64, v63, v147 op_sel:[0,0,0] op_sel_hi:[0,1,1]
	v_mfma_f32_32x32x16_f16 a[16:31], v[156:159], v[136:139], a[16:31]
	v_pk_mul_f16 v148, v72, v60 op_sel:[0,0] op_sel_hi:[0,1]
	v_pk_mul_f16 v149, v72, v61 op_sel:[0,0] op_sel_hi:[0,1]
	v_pk_mul_f16 v150, v72, v62 op_sel:[0,0] op_sel_hi:[0,1]
	v_pk_mul_f16 v151, v72, v63 op_sel:[0,0] op_sel_hi:[0,1]
	v_mfma_f32_32x32x16_f16 a[0:15], v[156:159], v[140:143], a[0:15]
	v_pk_fma_f16 v148, v64, v56, v148 op_sel:[0,0,0] op_sel_hi:[0,1,1] neg_lo:[0,0,1] neg_hi:[0,0,1]
	v_pk_fma_f16 v149, v64, v57, v149 op_sel:[0,0,0] op_sel_hi:[0,1,1] neg_lo:[0,0,1] neg_hi:[0,0,1]
	v_pk_fma_f16 v150, v64, v58, v150 op_sel:[0,0,0] op_sel_hi:[0,1,1] neg_lo:[0,0,1] neg_hi:[0,0,1]
	v_pk_fma_f16 v151, v64, v59, v151 op_sel:[0,0,0] op_sel_hi:[0,1,1] neg_lo:[0,0,1] neg_hi:[0,0,1]
	ds_read_b128 v[96:99], v161 offset:4096
	ds_read_b128 v[100:103], v161 offset:5120
	ds_read_b128 v[104:107], v161 offset:6144
	ds_read_b128 v[108:111], v161 offset:7168
	s_add_u32 s17, s17, 1
	s_cmp_eq_u32 s17, 17
	s_cbranch_scc1 .Lk2_epi

.Lk2_b10:
	s_waitcnt lgkmcnt(4)
	v_mfma_f32_32x32x16_f16 a[16:31], v[144:147], v[80:83], a[16:31]
	s_cmp_le_u32 s22, 16
	s_cselect_b32 s40, s18, 0x18000
	s_add_u32 m0, s40, s35
	s_add_u32 s22, s22, 1
	global_load_lds_dwordx4 v168, s[20:21]
	global_load_lds_dwordx4 v168, s[20:21] offset:1024
	v_pk_mul_f16 v152, v72, v56 op_sel:[1,0] op_sel_hi:[1,1]
	v_pk_mul_f16 v153, v72, v57 op_sel:[1,0] op_sel_hi:[1,1]
	v_pk_mul_f16 v154, v72, v58 op_sel:[1,0] op_sel_hi:[1,1]
	v_pk_mul_f16 v155, v72, v59 op_sel:[1,0] op_sel_hi:[1,1]
	v_mfma_f32_32x32x16_f16 a[0:15], v[144:147], v[84:87], a[0:15]
	s_cmp_le_u32 s22, 16
	s_cselect_b32 s41, 0x4000, 0
	s_add_u32 s20, s20, s41
	s_addc_u32 s21, s21, 0
	s_add_u32 s18, s18, 0x4000
	s_cmp_eq_u32 s18, 0x18000
	s_cselect_b32 s18, 0, s18
	v_pk_fma_f16 v152, v64, v60, v152 op_sel:[1,0,0] op_sel_hi:[1,1,1]
	v_pk_fma_f16 v153, v64, v61, v153 op_sel:[1,0,0] op_sel_hi:[1,1,1]
	v_pk_fma_f16 v154, v64, v62, v154 op_sel:[1,0,0] op_sel_hi:[1,1,1]
	v_pk_fma_f16 v155, v64, v63, v155 op_sel:[1,0,0] op_sel_hi:[1,1,1]
	v_mfma_f32_32x32x16_f16 a[16:31], v[148:151], v[88:91], a[16:31]
	v_pk_mul_f16 v156, v72, v60 op_sel:[1,0] op_sel_hi:[1,1]
	v_pk_mul_f16 v157, v72, v61 op_sel:[1,0] op_sel_hi:[1,1]
	v_pk_mul_f16 v158, v72, v62 op_sel:[1,0] op_sel_hi:[1,1]
	v_pk_mul_f16 v159, v72, v63 op_sel:[1,0] op_sel_hi:[1,1]
	v_mfma_f32_32x32x16_f16 a[0:15], v[148:151], v[92:95], a[0:15]
	v_pk_fma_f16 v156, v64, v56, v156 op_sel:[1,0,0] op_sel_hi:[1,1,1] neg_lo:[0,0,1] neg_hi:[0,0,1]
	v_pk_fma_f16 v157, v64, v57, v157 op_sel:[1,0,0] op_sel_hi:[1,1,1] neg_lo:[0,0,1] neg_hi:[0,0,1]
	v_pk_fma_f16 v158, v64, v58, v158 op_sel:[1,0,0] op_sel_hi:[1,1,1] neg_lo:[0,0,1] neg_hi:[0,0,1]
	v_pk_fma_f16 v159, v64, v59, v159 op_sel:[1,0,0] op_sel_hi:[1,1,1] neg_lo:[0,0,1] neg_hi:[0,0,1]
	ds_read_b128 v[112:115], v161 offset:8192
	ds_read_b128 v[116:119], v161 offset:9216
	ds_read_b128 v[120:123], v161 offset:10240
	ds_read_b128 v[124:127], v161 offset:11264
	s_waitcnt lgkmcnt(4)
	v_mfma_f32_32x32x16_f16 a[16:31], v[152:155], v[96:99], a[16:31]
	s_add_u32 s14, s14, 1
	s_cmp_eq_u32 s14, 16
	s_cselect_b32 s42, 1, 0
	s_add_u32 s13, s13, s42
	s_cmp_eq_u32 s42, 1
	s_cselect_b32 s14, s13, s14
	v_pk_mul_f16 v144, v73, v56 op_sel:[0,0] op_sel_hi:[0,1]
	v_pk_mul_f16 v145, v73, v57 op_sel:[0,0] op_sel_hi:[0,1]
	v_pk_mul_f16 v146, v73, v58 op_sel:[0,0] op_sel_hi:[0,1]
	v_pk_mul_f16 v147, v73, v59 op_sel:[0,0] op_sel_hi:[0,1]
	v_mfma_f32_32x32x16_f16 a[0:15], v[152:155], v[100:103], a[0:15]
	s_min_u32 s43, s13, 15
	s_min_u32 s44, s14, 15
	s_lshl_b32 s45, s44, 16
	s_add_u32 s24, s8, s45
	s_addc_u32 s25, s9, 0
	s_add_u32 s26, s24, 0x100000
	s_addc_u32 s27, s25, 0
	s_lshl_b32 s45, s43, 16
	s_add_u32 s28, s8, s45
	s_addc_u32 s29, s9, 0
	s_add_u32 s30, s28, 0x100000
	s_addc_u32 s31, s29, 0
	v_pk_fma_f16 v144, v65, v60, v144 op_sel:[0,0,0] op_sel_hi:[0,1,1]
	v_pk_fma_f16 v145, v65, v61, v145 op_sel:[0,0,0] op_sel_hi:[0,1,1]
	v_pk_fma_f16 v146, v65, v62, v146 op_sel:[0,0,0] op_sel_hi:[0,1,1]
	v_pk_fma_f16 v147, v65, v63, v147 op_sel:[0,0,0] op_sel_hi:[0,1,1]
	v_mfma_f32_32x32x16_f16 a[16:31], v[156:159], v[104:107], a[16:31]
	global_load_dwordx4 v[36:39], v164, s[24:25]
	global_load_dwordx4 v[32:35], v164, s[26:27]
	global_load_dwordx4 v[40:43], v165, s[28:29]
	global_load_dwordx4 v[44:47], v166, s[28:29]
	global_load_dwordx4 v[48:51], v165, s[30:31]
	global_load_dwordx4 v[52:55], v166, s[30:31]
	v_pk_mul_f16 v148, v73, v60 op_sel:[0,0] op_sel_hi:[0,1]
	v_pk_mul_f16 v149, v73, v61 op_sel:[0,0] op_sel_hi:[0,1]
	v_pk_mul_f16 v150, v73, v62 op_sel:[0,0] op_sel_hi:[0,1]
	v_pk_mul_f16 v151, v73, v63 op_sel:[0,0] op_sel_hi:[0,1]
	v_mfma_f32_32x32x16_f16 a[0:15], v[156:159], v[108:111], a[0:15]
	v_pk_fma_f16 v148, v65, v56, v148 op_sel:[0,0,0] op_sel_hi:[0,1,1] neg_lo:[0,0,1] neg_hi:[0,0,1]
	v_pk_fma_f16 v149, v65, v57, v149 op_sel:[0,0,0] op_sel_hi:[0,1,1] neg_lo:[0,0,1] neg_hi:[0,0,1]
	v_pk_fma_f16 v150, v65, v58, v150 op_sel:[0,0,0] op_sel_hi:[0,1,1] neg_lo:[0,0,1] neg_hi:[0,0,1]
	v_pk_fma_f16 v151, v65, v59, v151 op_sel:[0,0,0] op_sel_hi:[0,1,1] neg_lo:[0,0,1] neg_hi:[0,0,1]
	ds_read_b128 v[128:131], v161 offset:12288
	ds_read_b128 v[132:135], v161 offset:13312
	ds_read_b128 v[136:139], v161 offset:14336
	ds_read_b128 v[140:143], v161 offset:15360
	s_add_u32 s19, s19, 0x4000
	s_cmp_eq_u32 s19, 0x18000
	s_cselect_b32 s19, 0, s19
	v_add_u32_e32 v161, s19, v160
	s_waitcnt lgkmcnt(4)
	v_mfma_f32_32x32x16_f16 a[16:31], v[144:147], v[112:115], a[16:31]
	v_pk_mul_f16 v152, v73, v56 op_sel:[1,0] op_sel_hi:[1,1]
	v_pk_mul_f16 v153, v73, v57 op_sel:[1,0] op_sel_hi:[1,1]
	v_pk_mul_f16 v154, v73, v58 op_sel:[1,0] op_sel_hi:[1,1]
	v_pk_mul_f16 v155, v73, v59 op_sel:[1,0] op_sel_hi:[1,1]
	v_mfma_f32_32x32x16_f16 a[0:15], v[144:147], v[116:119], a[0:15]
	v_pk_fma_f16 v152, v65, v60, v152 op_sel:[1,0,0] op_sel_hi:[1,1,1]
	v_pk_fma_f16 v153, v65, v61, v153 op_sel:[1,0,0] op_sel_hi:[1,1,1]
	v_pk_fma_f16 v154, v65, v62, v154 op_sel:[1,0,0] op_sel_hi:[1,1,1]
	v_pk_fma_f16 v155, v65, v63, v155 op_sel:[1,0,0] op_sel_hi:[1,1,1]
	v_mfma_f32_32x32x16_f16 a[16:31], v[148:151], v[120:123], a[16:31]
	v_pk_mul_f16 v156, v73, v60 op_sel:[1,0] op_sel_hi:[1,1]
	v_pk_mul_f16 v157, v73, v61 op_sel:[1,0] op_sel_hi:[1,1]
	v_pk_mul_f16 v158, v73, v62 op_sel:[1,0] op_sel_hi:[1,1]
	v_pk_mul_f16 v159, v73, v63 op_sel:[1,0] op_sel_hi:[1,1]
	v_mfma_f32_32x32x16_f16 a[0:15], v[148:151], v[124:127], a[0:15]
	v_pk_fma_f16 v156, v65, v56, v156 op_sel:[1,0,0] op_sel_hi:[1,1,1] neg_lo:[0,0,1] neg_hi:[0,0,1]
	v_pk_fma_f16 v157, v65, v57, v157 op_sel:[1,0,0] op_sel_hi:[1,1,1] neg_lo:[0,0,1] neg_hi:[0,0,1]
	v_pk_fma_f16 v158, v65, v58, v158 op_sel:[1,0,0] op_sel_hi:[1,1,1] neg_lo:[0,0,1] neg_hi:[0,0,1]
	v_pk_fma_f16 v159, v65, v59, v159 op_sel:[1,0,0] op_sel_hi:[1,1,1] neg_lo:[0,0,1] neg_hi:[0,0,1]
	ds_read_b128 v[80:83], v161
	ds_read_b128 v[84:87], v161 offset:1024
	ds_read_b128 v[88:91], v161 offset:2048
	ds_read_b128 v[92:95], v161 offset:3072
	s_waitcnt lgkmcnt(4)
	v_mfma_f32_32x32x16_f16 a[16:31], v[152:155], v[128:131], a[16:31]
	v_pk_mul_f16 v144, v74, v56 op_sel:[0,0] op_sel_hi:[0,1]
	v_pk_mul_f16 v145, v74, v57 op_sel:[0,0] op_sel_hi:[0,1]
	v_pk_mul_f16 v146, v74, v58 op_sel:[0,0] op_sel_hi:[0,1]
	v_pk_mul_f16 v147, v74, v59 op_sel:[0,0] op_sel_hi:[0,1]
	v_mfma_f32_32x32x16_f16 a[0:15], v[152:155], v[132:135], a[0:15]
	v_pk_fma_f16 v144, v66, v60, v144 op_sel:[0,0,0] op_sel_hi:[0,1,1]
	v_pk_fma_f16 v145, v66, v61, v145 op_sel:[0,0,0] op_sel_hi:[0,1,1]
	v_pk_fma_f16 v146, v66, v62, v146 op_sel:[0,0,0] op_sel_hi:[0,1,1]
	v_pk_fma_f16 v147, v66, v63, v147 op_sel:[0,0,0] op_sel_hi:[0,1,1]
	v_mfma_f32_32x32x16_f16 a[16:31], v[156:159], v[136:139], a[16:31]
	v_pk_mul_f16 v148, v74, v60 op_sel:[0,0] op_sel_hi:[0,1]
	v_pk_mul_f16 v149, v74, v61 op_sel:[0,0] op_sel_hi:[0,1]
	v_pk_mul_f16 v150, v74, v62 op_sel:[0,0] op_sel_hi:[0,1]
	v_pk_mul_f16 v151, v74, v63 op_sel:[0,0] op_sel_hi:[0,1]
	v_mfma_f32_32x32x16_f16 a[0:15], v[156:159], v[140:143], a[0:15]
	v_pk_fma_f16 v148, v66, v56, v148 op_sel:[0,0,0] op_sel_hi:[0,1,1] neg_lo:[0,0,1] neg_hi:[0,0,1]
	v_pk_fma_f16 v149, v66, v57, v149 op_sel:[0,0,0] op_sel_hi:[0,1,1] neg_lo:[0,0,1] neg_hi:[0,0,1]
	v_pk_fma_f16 v150, v66, v58, v150 op_sel:[0,0,0] op_sel_hi:[0,1,1] neg_lo:[0,0,1] neg_hi:[0,0,1]
	v_pk_fma_f16 v151, v66, v59, v151 op_sel:[0,0,0] op_sel_hi:[0,1,1] neg_lo:[0,0,1] neg_hi:[0,0,1]
	ds_read_b128 v[96:99], v161 offset:4096
	ds_read_b128 v[100:103], v161 offset:5120
	ds_read_b128 v[104:107], v161 offset:6144
	ds_read_b128 v[108:111], v161 offset:7168
	s_add_u32 s17, s17, 1
	s_cmp_eq_u32 s17, 17
	s_cbranch_scc1 .Lk2_epi

.Lk2_b11:
	s_waitcnt lgkmcnt(4)
	v_mfma_f32_32x32x16_f16 a[16:31], v[144:147], v[80:83], a[16:31]
	s_cmp_le_u32 s22, 16
	s_cselect_b32 s40, s18, 0x18000
	s_add_u32 m0, s40, s35
	s_add_u32 s22, s22, 1
	global_load_lds_dwordx4 v168, s[20:21]
	global_load_lds_dwordx4 v168, s[20:21] offset:1024
	v_pk_mul_f16 v152, v74, v56 op_sel:[1,0] op_sel_hi:[1,1]
	v_pk_mul_f16 v153, v74, v57 op_sel:[1,0] op_sel_hi:[1,1]
	v_pk_mul_f16 v154, v74, v58 op_sel:[1,0] op_sel_hi:[1,1]
	v_pk_mul_f16 v155, v74, v59 op_sel:[1,0] op_sel_hi:[1,1]
	v_mfma_f32_32x32x16_f16 a[0:15], v[144:147], v[84:87], a[0:15]
	s_cmp_le_u32 s22, 16
	s_cselect_b32 s41, 0x4000, 0
	s_add_u32 s20, s20, s41
	s_addc_u32 s21, s21, 0
	s_add_u32 s18, s18, 0x4000
	s_cmp_eq_u32 s18, 0x18000
	s_cselect_b32 s18, 0, s18
	v_pk_fma_f16 v152, v66, v60, v152 op_sel:[1,0,0] op_sel_hi:[1,1,1]
	v_pk_fma_f16 v153, v66, v61, v153 op_sel:[1,0,0] op_sel_hi:[1,1,1]
	v_pk_fma_f16 v154, v66, v62, v154 op_sel:[1,0,0] op_sel_hi:[1,1,1]
	v_pk_fma_f16 v155, v66, v63, v155 op_sel:[1,0,0] op_sel_hi:[1,1,1]
	v_mfma_f32_32x32x16_f16 a[16:31], v[148:151], v[88:91], a[16:31]
	v_pk_mul_f16 v156, v74, v60 op_sel:[1,0] op_sel_hi:[1,1]
	v_pk_mul_f16 v157, v74, v61 op_sel:[1,0] op_sel_hi:[1,1]
	v_pk_mul_f16 v158, v74, v62 op_sel:[1,0] op_sel_hi:[1,1]
	v_pk_mul_f16 v159, v74, v63 op_sel:[1,0] op_sel_hi:[1,1]
	v_mfma_f32_32x32x16_f16 a[0:15], v[148:151], v[92:95], a[0:15]
	v_pk_fma_f16 v156, v66, v56, v156 op_sel:[1,0,0] op_sel_hi:[1,1,1] neg_lo:[0,0,1] neg_hi:[0,0,1]
	v_pk_fma_f16 v157, v66, v57, v157 op_sel:[1,0,0] op_sel_hi:[1,1,1] neg_lo:[0,0,1] neg_hi:[0,0,1]
	v_pk_fma_f16 v158, v66, v58, v158 op_sel:[1,0,0] op_sel_hi:[1,1,1] neg_lo:[0,0,1] neg_hi:[0,0,1]
	v_pk_fma_f16 v159, v66, v59, v159 op_sel:[1,0,0] op_sel_hi:[1,1,1] neg_lo:[0,0,1] neg_hi:[0,0,1]
	ds_read_b128 v[112:115], v161 offset:8192
	ds_read_b128 v[116:119], v161 offset:9216
	ds_read_b128 v[120:123], v161 offset:10240
	ds_read_b128 v[124:127], v161 offset:11264
	s_waitcnt lgkmcnt(4)
	v_mfma_f32_32x32x16_f16 a[16:31], v[152:155], v[96:99], a[16:31]
	v_pk_mul_f16 v144, v75, v56 op_sel:[0,0] op_sel_hi:[0,1]
	v_pk_mul_f16 v145, v75, v57 op_sel:[0,0] op_sel_hi:[0,1]
	v_pk_mul_f16 v146, v75, v58 op_sel:[0,0] op_sel_hi:[0,1]
	v_pk_mul_f16 v147, v75, v59 op_sel:[0,0] op_sel_hi:[0,1]
	v_mfma_f32_32x32x16_f16 a[0:15], v[152:155], v[100:103], a[0:15]
	v_pk_fma_f16 v144, v67, v60, v144 op_sel:[0,0,0] op_sel_hi:[0,1,1]
	v_pk_fma_f16 v145, v67, v61, v145 op_sel:[0,0,0] op_sel_hi:[0,1,1]
	v_pk_fma_f16 v146, v67, v62, v146 op_sel:[0,0,0] op_sel_hi:[0,1,1]
	v_pk_fma_f16 v147, v67, v63, v147 op_sel:[0,0,0] op_sel_hi:[0,1,1]
	v_mfma_f32_32x32x16_f16 a[16:31], v[156:159], v[104:107], a[16:31]
	v_pk_mul_f16 v148, v75, v60 op_sel:[0,0] op_sel_hi:[0,1]
	v_pk_mul_f16 v149, v75, v61 op_sel:[0,0] op_sel_hi:[0,1]
	v_pk_mul_f16 v150, v75, v62 op_sel:[0,0] op_sel_hi:[0,1]
	v_pk_mul_f16 v151, v75, v63 op_sel:[0,0] op_sel_hi:[0,1]
	v_mfma_f32_32x32x16_f16 a[0:15], v[156:159], v[108:111], a[0:15]
	v_pk_fma_f16 v148, v67, v56, v148 op_sel:[0,0,0] op_sel_hi:[0,1,1] neg_lo:[0,0,1] neg_hi:[0,0,1]
	v_pk_fma_f16 v149, v67, v57, v149 op_sel:[0,0,0] op_sel_hi:[0,1,1] neg_lo:[0,0,1] neg_hi:[0,0,1]
	v_pk_fma_f16 v150, v67, v58, v150 op_sel:[0,0,0] op_sel_hi:[0,1,1] neg_lo:[0,0,1] neg_hi:[0,0,1]
	v_pk_fma_f16 v151, v67, v59, v151 op_sel:[0,0,0] op_sel_hi:[0,1,1] neg_lo:[0,0,1] neg_hi:[0,0,1]
	ds_read_b128 v[128:131], v161 offset:12288
	ds_read_b128 v[132:135], v161 offset:13312
	ds_read_b128 v[136:139], v161 offset:14336
	ds_read_b128 v[140:143], v161 offset:15360
	s_add_u32 s19, s19, 0x4000
	s_cmp_eq_u32 s19, 0x18000
	s_cselect_b32 s19, 0, s19
	v_add_u32_e32 v161, s19, v160
	s_waitcnt lgkmcnt(4)
	v_mfma_f32_32x32x16_f16 a[16:31], v[144:147], v[112:115], a[16:31]
	v_pk_mul_f16 v152, v75, v56 op_sel:[1,0] op_sel_hi:[1,1]
	v_pk_mul_f16 v153, v75, v57 op_sel:[1,0] op_sel_hi:[1,1]
	v_pk_mul_f16 v154, v75, v58 op_sel:[1,0] op_sel_hi:[1,1]
	v_pk_mul_f16 v155, v75, v59 op_sel:[1,0] op_sel_hi:[1,1]
	v_mfma_f32_32x32x16_f16 a[0:15], v[144:147], v[116:119], a[0:15]
	v_pk_fma_f16 v152, v67, v60, v152 op_sel:[1,0,0] op_sel_hi:[1,1,1]
	v_pk_fma_f16 v153, v67, v61, v153 op_sel:[1,0,0] op_sel_hi:[1,1,1]
	v_pk_fma_f16 v154, v67, v62, v154 op_sel:[1,0,0] op_sel_hi:[1,1,1]
	v_pk_fma_f16 v155, v67, v63, v155 op_sel:[1,0,0] op_sel_hi:[1,1,1]
	v_mfma_f32_32x32x16_f16 a[16:31], v[148:151], v[120:123], a[16:31]
	v_pk_mul_f16 v156, v75, v60 op_sel:[1,0] op_sel_hi:[1,1]
	v_pk_mul_f16 v157, v75, v61 op_sel:[1,0] op_sel_hi:[1,1]
	v_pk_mul_f16 v158, v75, v62 op_sel:[1,0] op_sel_hi:[1,1]
	v_pk_mul_f16 v159, v75, v63 op_sel:[1,0] op_sel_hi:[1,1]
	v_mfma_f32_32x32x16_f16 a[0:15], v[148:151], v[124:127], a[0:15]
	v_pk_fma_f16 v156, v67, v56, v156 op_sel:[1,0,0] op_sel_hi:[1,1,1] neg_lo:[0,0,1] neg_hi:[0,0,1]
	v_pk_fma_f16 v157, v67, v57, v157 op_sel:[1,0,0] op_sel_hi:[1,1,1] neg_lo:[0,0,1] neg_hi:[0,0,1]
	v_pk_fma_f16 v158, v67, v58, v158 op_sel:[1,0,0] op_sel_hi:[1,1,1] neg_lo:[0,0,1] neg_hi:[0,0,1]
	v_pk_fma_f16 v159, v67, v59, v159 op_sel:[1,0,0] op_sel_hi:[1,1,1] neg_lo:[0,0,1] neg_hi:[0,0,1]
	ds_read_b128 v[80:83], v161
	ds_read_b128 v[84:87], v161 offset:1024
	ds_read_b128 v[88:91], v161 offset:2048
	ds_read_b128 v[92:95], v161 offset:3072
	s_waitcnt lgkmcnt(4)
	v_mfma_f32_32x32x16_f16 a[16:31], v[152:155], v[128:131], a[16:31]
	v_pk_mul_f16 v144, v76, v56 op_sel:[0,0] op_sel_hi:[0,1]
	v_pk_mul_f16 v145, v76, v57 op_sel:[0,0] op_sel_hi:[0,1]
	v_pk_mul_f16 v146, v76, v58 op_sel:[0,0] op_sel_hi:[0,1]
	v_pk_mul_f16 v147, v76, v59 op_sel:[0,0] op_sel_hi:[0,1]
	v_mfma_f32_32x32x16_f16 a[0:15], v[152:155], v[132:135], a[0:15]
	v_pk_fma_f16 v144, v68, v60, v144 op_sel:[0,0,0] op_sel_hi:[0,1,1]
	v_pk_fma_f16 v145, v68, v61, v145 op_sel:[0,0,0] op_sel_hi:[0,1,1]
	v_pk_fma_f16 v146, v68, v62, v146 op_sel:[0,0,0] op_sel_hi:[0,1,1]
	v_pk_fma_f16 v147, v68, v63, v147 op_sel:[0,0,0] op_sel_hi:[0,1,1]
	v_mfma_f32_32x32x16_f16 a[16:31], v[156:159], v[136:139], a[16:31]
	v_pk_mul_f16 v148, v76, v60 op_sel:[0,0] op_sel_hi:[0,1]
	v_pk_mul_f16 v149, v76, v61 op_sel:[0,0] op_sel_hi:[0,1]
	v_pk_mul_f16 v150, v76, v62 op_sel:[0,0] op_sel_hi:[0,1]
	v_pk_mul_f16 v151, v76, v63 op_sel:[0,0] op_sel_hi:[0,1]
	v_mfma_f32_32x32x16_f16 a[0:15], v[156:159], v[140:143], a[0:15]
	v_pk_fma_f16 v148, v68, v56, v148 op_sel:[0,0,0] op_sel_hi:[0,1,1] neg_lo:[0,0,1] neg_hi:[0,0,1]
	v_pk_fma_f16 v149, v68, v57, v149 op_sel:[0,0,0] op_sel_hi:[0,1,1] neg_lo:[0,0,1] neg_hi:[0,0,1]
	v_pk_fma_f16 v150, v68, v58, v150 op_sel:[0,0,0] op_sel_hi:[0,1,1] neg_lo:[0,0,1] neg_hi:[0,0,1]
	v_pk_fma_f16 v151, v68, v59, v151 op_sel:[0,0,0] op_sel_hi:[0,1,1] neg_lo:[0,0,1] neg_hi:[0,0,1]
	ds_read_b128 v[96:99], v161 offset:4096
	ds_read_b128 v[100:103], v161 offset:5120
	ds_read_b128 v[104:107], v161 offset:6144
	ds_read_b128 v[108:111], v161 offset:7168
	s_add_u32 s17, s17, 1
	s_cmp_eq_u32 s17, 17
	s_cbranch_scc1 .Lk2_epi

.Lk2_b12:
	s_waitcnt lgkmcnt(4)
	v_mfma_f32_32x32x16_f16 a[16:31], v[144:147], v[80:83], a[16:31]
	s_cmp_le_u32 s22, 16
	s_cselect_b32 s40, s18, 0x18000
	s_add_u32 m0, s40, s35
	s_add_u32 s22, s22, 1
	global_load_lds_dwordx4 v168, s[20:21]
	global_load_lds_dwordx4 v168, s[20:21] offset:1024
	v_pk_mul_f16 v152, v76, v56 op_sel:[1,0] op_sel_hi:[1,1]
	v_pk_mul_f16 v153, v76, v57 op_sel:[1,0] op_sel_hi:[1,1]
	v_pk_mul_f16 v154, v76, v58 op_sel:[1,0] op_sel_hi:[1,1]
	v_pk_mul_f16 v155, v76, v59 op_sel:[1,0] op_sel_hi:[1,1]
	v_mfma_f32_32x32x16_f16 a[0:15], v[144:147], v[84:87], a[0:15]
	s_cmp_le_u32 s22, 16
	s_cselect_b32 s41, 0x4000, 0
	s_add_u32 s20, s20, s41
	s_addc_u32 s21, s21, 0
	s_add_u32 s18, s18, 0x4000
	s_cmp_eq_u32 s18, 0x18000
	s_cselect_b32 s18, 0, s18
	v_pk_fma_f16 v152, v68, v60, v152 op_sel:[1,0,0] op_sel_hi:[1,1,1]
	v_pk_fma_f16 v153, v68, v61, v153 op_sel:[1,0,0] op_sel_hi:[1,1,1]
	v_pk_fma_f16 v154, v68, v62, v154 op_sel:[1,0,0] op_sel_hi:[1,1,1]
	v_pk_fma_f16 v155, v68, v63, v155 op_sel:[1,0,0] op_sel_hi:[1,1,1]
	v_mfma_f32_32x32x16_f16 a[16:31], v[148:151], v[88:91], a[16:31]
	v_pk_mul_f16 v156, v76, v60 op_sel:[1,0] op_sel_hi:[1,1]
	v_pk_mul_f16 v157, v76, v61 op_sel:[1,0] op_sel_hi:[1,1]
	v_pk_mul_f16 v158, v76, v62 op_sel:[1,0] op_sel_hi:[1,1]
	v_pk_mul_f16 v159, v76, v63 op_sel:[1,0] op_sel_hi:[1,1]
	v_mfma_f32_32x32x16_f16 a[0:15], v[148:151], v[92:95], a[0:15]
	v_pk_fma_f16 v156, v68, v56, v156 op_sel:[1,0,0] op_sel_hi:[1,1,1] neg_lo:[0,0,1] neg_hi:[0,0,1]
	v_pk_fma_f16 v157, v68, v57, v157 op_sel:[1,0,0] op_sel_hi:[1,1,1] neg_lo:[0,0,1] neg_hi:[0,0,1]
	v_pk_fma_f16 v158, v68, v58, v158 op_sel:[1,0,0] op_sel_hi:[1,1,1] neg_lo:[0,0,1] neg_hi:[0,0,1]
	v_pk_fma_f16 v159, v68, v59, v159 op_sel:[1,0,0] op_sel_hi:[1,1,1] neg_lo:[0,0,1] neg_hi:[0,0,1]
	ds_read_b128 v[112:115], v161 offset:8192
	ds_read_b128 v[116:119], v161 offset:9216
	ds_read_b128 v[120:123], v161 offset:10240
	ds_read_b128 v[124:127], v161 offset:11264
	s_waitcnt lgkmcnt(4)
	v_mfma_f32_32x32x16_f16 a[16:31], v[152:155], v[96:99], a[16:31]
	v_pk_mul_f16 v144, v77, v56 op_sel:[0,0] op_sel_hi:[0,1]
	v_pk_mul_f16 v145, v77, v57 op_sel:[0,0] op_sel_hi:[0,1]
	v_pk_mul_f16 v146, v77, v58 op_sel:[0,0] op_sel_hi:[0,1]
	v_pk_mul_f16 v147, v77, v59 op_sel:[0,0] op_sel_hi:[0,1]
	v_mfma_f32_32x32x16_f16 a[0:15], v[152:155], v[100:103], a[0:15]
	v_pk_fma_f16 v144, v69, v60, v144 op_sel:[0,0,0] op_sel_hi:[0,1,1]
	v_pk_fma_f16 v145, v69, v61, v145 op_sel:[0,0,0] op_sel_hi:[0,1,1]
	v_pk_fma_f16 v146, v69, v62, v146 op_sel:[0,0,0] op_sel_hi:[0,1,1]
	v_pk_fma_f16 v147, v69, v63, v147 op_sel:[0,0,0] op_sel_hi:[0,1,1]
	v_mfma_f32_32x32x16_f16 a[16:31], v[156:159], v[104:107], a[16:31]
	v_pk_mul_f16 v148, v77, v60 op_sel:[0,0] op_sel_hi:[0,1]
	v_pk_mul_f16 v149, v77, v61 op_sel:[0,0] op_sel_hi:[0,1]
	v_pk_mul_f16 v150, v77, v62 op_sel:[0,0] op_sel_hi:[0,1]
	v_pk_mul_f16 v151, v77, v63 op_sel:[0,0] op_sel_hi:[0,1]
	v_mfma_f32_32x32x16_f16 a[0:15], v[156:159], v[108:111], a[0:15]
	v_pk_fma_f16 v148, v69, v56, v148 op_sel:[0,0,0] op_sel_hi:[0,1,1] neg_lo:[0,0,1] neg_hi:[0,0,1]
	v_pk_fma_f16 v149, v69, v57, v149 op_sel:[0,0,0] op_sel_hi:[0,1,1] neg_lo:[0,0,1] neg_hi:[0,0,1]
	v_pk_fma_f16 v150, v69, v58, v150 op_sel:[0,0,0] op_sel_hi:[0,1,1] neg_lo:[0,0,1] neg_hi:[0,0,1]
	v_pk_fma_f16 v151, v69, v59, v151 op_sel:[0,0,0] op_sel_hi:[0,1,1] neg_lo:[0,0,1] neg_hi:[0,0,1]
	ds_read_b128 v[128:131], v161 offset:12288
	ds_read_b128 v[132:135], v161 offset:13312
	ds_read_b128 v[136:139], v161 offset:14336
	ds_read_b128 v[140:143], v161 offset:15360
	s_add_u32 s19, s19, 0x4000
	s_cmp_eq_u32 s19, 0x18000
	s_cselect_b32 s19, 0, s19
	v_add_u32_e32 v161, s19, v160
	s_waitcnt lgkmcnt(4)
	v_mfma_f32_32x32x16_f16 a[16:31], v[144:147], v[112:115], a[16:31]
	v_pk_mul_f16 v152, v77, v56 op_sel:[1,0] op_sel_hi:[1,1]
	v_pk_mul_f16 v153, v77, v57 op_sel:[1,0] op_sel_hi:[1,1]
	v_pk_mul_f16 v154, v77, v58 op_sel:[1,0] op_sel_hi:[1,1]
	v_pk_mul_f16 v155, v77, v59 op_sel:[1,0] op_sel_hi:[1,1]
	v_mfma_f32_32x32x16_f16 a[0:15], v[144:147], v[116:119], a[0:15]
	v_pk_fma_f16 v152, v69, v60, v152 op_sel:[1,0,0] op_sel_hi:[1,1,1]
	v_pk_fma_f16 v153, v69, v61, v153 op_sel:[1,0,0] op_sel_hi:[1,1,1]
	v_pk_fma_f16 v154, v69, v62, v154 op_sel:[1,0,0] op_sel_hi:[1,1,1]
	v_pk_fma_f16 v155, v69, v63, v155 op_sel:[1,0,0] op_sel_hi:[1,1,1]
	v_mfma_f32_32x32x16_f16 a[16:31], v[148:151], v[120:123], a[16:31]
	v_pk_mul_f16 v156, v77, v60 op_sel:[1,0] op_sel_hi:[1,1]
	v_pk_mul_f16 v157, v77, v61 op_sel:[1,0] op_sel_hi:[1,1]
	v_pk_mul_f16 v158, v77, v62 op_sel:[1,0] op_sel_hi:[1,1]
	v_pk_mul_f16 v159, v77, v63 op_sel:[1,0] op_sel_hi:[1,1]
	v_mfma_f32_32x32x16_f16 a[0:15], v[148:151], v[124:127], a[0:15]
	v_pk_fma_f16 v156, v69, v56, v156 op_sel:[1,0,0] op_sel_hi:[1,1,1] neg_lo:[0,0,1] neg_hi:[0,0,1]
	v_pk_fma_f16 v157, v69, v57, v157 op_sel:[1,0,0] op_sel_hi:[1,1,1] neg_lo:[0,0,1] neg_hi:[0,0,1]
	v_pk_fma_f16 v158, v69, v58, v158 op_sel:[1,0,0] op_sel_hi:[1,1,1] neg_lo:[0,0,1] neg_hi:[0,0,1]
	v_pk_fma_f16 v159, v69, v59, v159 op_sel:[1,0,0] op_sel_hi:[1,1,1] neg_lo:[0,0,1] neg_hi:[0,0,1]
	ds_read_b128 v[80:83], v161
	ds_read_b128 v[84:87], v161 offset:1024
	ds_read_b128 v[88:91], v161 offset:2048
	ds_read_b128 v[92:95], v161 offset:3072
	s_waitcnt lgkmcnt(4)
	v_mfma_f32_32x32x16_f16 a[16:31], v[152:155], v[128:131], a[16:31]
	v_pk_mul_f16 v144, v78, v56 op_sel:[0,0] op_sel_hi:[0,1]
	v_pk_mul_f16 v145, v78, v57 op_sel:[0,0] op_sel_hi:[0,1]
	v_pk_mul_f16 v146, v78, v58 op_sel:[0,0] op_sel_hi:[0,1]
	v_pk_mul_f16 v147, v78, v59 op_sel:[0,0] op_sel_hi:[0,1]
	v_mfma_f32_32x32x16_f16 a[0:15], v[152:155], v[132:135], a[0:15]
	v_pk_fma_f16 v144, v70, v60, v144 op_sel:[0,0,0] op_sel_hi:[0,1,1]
	v_pk_fma_f16 v145, v70, v61, v145 op_sel:[0,0,0] op_sel_hi:[0,1,1]
	v_pk_fma_f16 v146, v70, v62, v146 op_sel:[0,0,0] op_sel_hi:[0,1,1]
	v_pk_fma_f16 v147, v70, v63, v147 op_sel:[0,0,0] op_sel_hi:[0,1,1]
	v_mfma_f32_32x32x16_f16 a[16:31], v[156:159], v[136:139], a[16:31]
	v_pk_mul_f16 v148, v78, v60 op_sel:[0,0] op_sel_hi:[0,1]
	v_pk_mul_f16 v149, v78, v61 op_sel:[0,0] op_sel_hi:[0,1]
	v_pk_mul_f16 v150, v78, v62 op_sel:[0,0] op_sel_hi:[0,1]
	v_pk_mul_f16 v151, v78, v63 op_sel:[0,0] op_sel_hi:[0,1]
	v_mfma_f32_32x32x16_f16 a[0:15], v[156:159], v[140:143], a[0:15]
	v_pk_fma_f16 v148, v70, v56, v148 op_sel:[0,0,0] op_sel_hi:[0,1,1] neg_lo:[0,0,1] neg_hi:[0,0,1]
	v_pk_fma_f16 v149, v70, v57, v149 op_sel:[0,0,0] op_sel_hi:[0,1,1] neg_lo:[0,0,1] neg_hi:[0,0,1]
	v_pk_fma_f16 v150, v70, v58, v150 op_sel:[0,0,0] op_sel_hi:[0,1,1] neg_lo:[0,0,1] neg_hi:[0,0,1]
	v_pk_fma_f16 v151, v70, v59, v151 op_sel:[0,0,0] op_sel_hi:[0,1,1] neg_lo:[0,0,1] neg_hi:[0,0,1]
	ds_read_b128 v[96:99], v161 offset:4096
	ds_read_b128 v[100:103], v161 offset:5120
	ds_read_b128 v[104:107], v161 offset:6144
	ds_read_b128 v[108:111], v161 offset:7168
	s_add_u32 s17, s17, 1
	s_cmp_eq_u32 s17, 17
	s_cbranch_scc1 .Lk2_epi

.Lk2_b13:
	s_waitcnt lgkmcnt(4)
	v_mfma_f32_32x32x16_f16 a[16:31], v[144:147], v[80:83], a[16:31]
	s_cmp_le_u32 s22, 16
	s_cselect_b32 s40, s18, 0x18000
	s_add_u32 m0, s40, s35
	s_add_u32 s22, s22, 1
	global_load_lds_dwordx4 v168, s[20:21]
	global_load_lds_dwordx4 v168, s[20:21] offset:1024
	v_pk_mul_f16 v152, v78, v56 op_sel:[1,0] op_sel_hi:[1,1]
	v_pk_mul_f16 v153, v78, v57 op_sel:[1,0] op_sel_hi:[1,1]
	v_pk_mul_f16 v154, v78, v58 op_sel:[1,0] op_sel_hi:[1,1]
	v_pk_mul_f16 v155, v78, v59 op_sel:[1,0] op_sel_hi:[1,1]
	v_mfma_f32_32x32x16_f16 a[0:15], v[144:147], v[84:87], a[0:15]
	s_cmp_le_u32 s22, 16
	s_cselect_b32 s41, 0x4000, 0
	s_add_u32 s20, s20, s41
	s_addc_u32 s21, s21, 0
	s_add_u32 s18, s18, 0x4000
	s_cmp_eq_u32 s18, 0x18000
	s_cselect_b32 s18, 0, s18
	v_pk_fma_f16 v152, v70, v60, v152 op_sel:[1,0,0] op_sel_hi:[1,1,1]
	v_pk_fma_f16 v153, v70, v61, v153 op_sel:[1,0,0] op_sel_hi:[1,1,1]
	v_pk_fma_f16 v154, v70, v62, v154 op_sel:[1,0,0] op_sel_hi:[1,1,1]
	v_pk_fma_f16 v155, v70, v63, v155 op_sel:[1,0,0] op_sel_hi:[1,1,1]
	v_mfma_f32_32x32x16_f16 a[16:31], v[148:151], v[88:91], a[16:31]
	v_pk_mul_f16 v156, v78, v60 op_sel:[1,0] op_sel_hi:[1,1]
	v_pk_mul_f16 v157, v78, v61 op_sel:[1,0] op_sel_hi:[1,1]
	v_pk_mul_f16 v158, v78, v62 op_sel:[1,0] op_sel_hi:[1,1]
	v_pk_mul_f16 v159, v78, v63 op_sel:[1,0] op_sel_hi:[1,1]
	v_mfma_f32_32x32x16_f16 a[0:15], v[148:151], v[92:95], a[0:15]
	v_pk_fma_f16 v156, v70, v56, v156 op_sel:[1,0,0] op_sel_hi:[1,1,1] neg_lo:[0,0,1] neg_hi:[0,0,1]
	v_pk_fma_f16 v157, v70, v57, v157 op_sel:[1,0,0] op_sel_hi:[1,1,1] neg_lo:[0,0,1] neg_hi:[0,0,1]
	v_pk_fma_f16 v158, v70, v58, v158 op_sel:[1,0,0] op_sel_hi:[1,1,1] neg_lo:[0,0,1] neg_hi:[0,0,1]
	v_pk_fma_f16 v159, v70, v59, v159 op_sel:[1,0,0] op_sel_hi:[1,1,1] neg_lo:[0,0,1] neg_hi:[0,0,1]
	ds_read_b128 v[112:115], v161 offset:8192
	ds_read_b128 v[116:119], v161 offset:9216
	ds_read_b128 v[120:123], v161 offset:10240
	ds_read_b128 v[124:127], v161 offset:11264
	s_waitcnt lgkmcnt(4)
	v_mfma_f32_32x32x16_f16 a[16:31], v[152:155], v[96:99], a[16:31]
	v_pk_mul_f16 v144, v79, v56 op_sel:[0,0] op_sel_hi:[0,1]
	v_pk_mul_f16 v145, v79, v57 op_sel:[0,0] op_sel_hi:[0,1]
	v_pk_mul_f16 v146, v79, v58 op_sel:[0,0] op_sel_hi:[0,1]
	v_pk_mul_f16 v147, v79, v59 op_sel:[0,0] op_sel_hi:[0,1]
	v_mfma_f32_32x32x16_f16 a[0:15], v[152:155], v[100:103], a[0:15]
	v_pk_fma_f16 v144, v71, v60, v144 op_sel:[0,0,0] op_sel_hi:[0,1,1]
	v_pk_fma_f16 v145, v71, v61, v145 op_sel:[0,0,0] op_sel_hi:[0,1,1]
	v_pk_fma_f16 v146, v71, v62, v146 op_sel:[0,0,0] op_sel_hi:[0,1,1]
	v_pk_fma_f16 v147, v71, v63, v147 op_sel:[0,0,0] op_sel_hi:[0,1,1]
	v_mfma_f32_32x32x16_f16 a[16:31], v[156:159], v[104:107], a[16:31]
	v_pk_mul_f16 v148, v79, v60 op_sel:[0,0] op_sel_hi:[0,1]
	v_pk_mul_f16 v149, v79, v61 op_sel:[0,0] op_sel_hi:[0,1]
	v_pk_mul_f16 v150, v79, v62 op_sel:[0,0] op_sel_hi:[0,1]
	v_pk_mul_f16 v151, v79, v63 op_sel:[0,0] op_sel_hi:[0,1]
	v_mfma_f32_32x32x16_f16 a[0:15], v[156:159], v[108:111], a[0:15]
	v_pk_fma_f16 v148, v71, v56, v148 op_sel:[0,0,0] op_sel_hi:[0,1,1] neg_lo:[0,0,1] neg_hi:[0,0,1]
	v_pk_fma_f16 v149, v71, v57, v149 op_sel:[0,0,0] op_sel_hi:[0,1,1] neg_lo:[0,0,1] neg_hi:[0,0,1]
	v_pk_fma_f16 v150, v71, v58, v150 op_sel:[0,0,0] op_sel_hi:[0,1,1] neg_lo:[0,0,1] neg_hi:[0,0,1]
	v_pk_fma_f16 v151, v71, v59, v151 op_sel:[0,0,0] op_sel_hi:[0,1,1] neg_lo:[0,0,1] neg_hi:[0,0,1]
	ds_read_b128 v[128:131], v161 offset:12288
	ds_read_b128 v[132:135], v161 offset:13312
	ds_read_b128 v[136:139], v161 offset:14336
	ds_read_b128 v[140:143], v161 offset:15360
	s_add_u32 s19, s19, 0x4000
	s_cmp_eq_u32 s19, 0x18000
	s_cselect_b32 s19, 0, s19
	v_add_u32_e32 v161, s19, v160
	s_waitcnt lgkmcnt(4)
	v_mfma_f32_32x32x16_f16 a[16:31], v[144:147], v[112:115], a[16:31]
	v_pk_mul_f16 v152, v79, v56 op_sel:[1,0] op_sel_hi:[1,1]
	v_pk_mul_f16 v153, v79, v57 op_sel:[1,0] op_sel_hi:[1,1]
	v_pk_mul_f16 v154, v79, v58 op_sel:[1,0] op_sel_hi:[1,1]
	v_pk_mul_f16 v155, v79, v59 op_sel:[1,0] op_sel_hi:[1,1]
	v_mfma_f32_32x32x16_f16 a[0:15], v[144:147], v[116:119], a[0:15]
	v_pk_fma_f16 v152, v71, v60, v152 op_sel:[1,0,0] op_sel_hi:[1,1,1]
	v_pk_fma_f16 v153, v71, v61, v153 op_sel:[1,0,0] op_sel_hi:[1,1,1]
	v_pk_fma_f16 v154, v71, v62, v154 op_sel:[1,0,0] op_sel_hi:[1,1,1]
	v_pk_fma_f16 v155, v71, v63, v155 op_sel:[1,0,0] op_sel_hi:[1,1,1]
	v_mfma_f32_32x32x16_f16 a[16:31], v[148:151], v[120:123], a[16:31]
	v_pk_mul_f16 v156, v79, v60 op_sel:[1,0] op_sel_hi:[1,1]
	v_pk_mul_f16 v157, v79, v61 op_sel:[1,0] op_sel_hi:[1,1]
	v_pk_mul_f16 v158, v79, v62 op_sel:[1,0] op_sel_hi:[1,1]
	v_pk_mul_f16 v159, v79, v63 op_sel:[1,0] op_sel_hi:[1,1]
	v_mfma_f32_32x32x16_f16 a[0:15], v[148:151], v[124:127], a[0:15]
	v_pk_fma_f16 v156, v71, v56, v156 op_sel:[1,0,0] op_sel_hi:[1,1,1] neg_lo:[0,0,1] neg_hi:[0,0,1]
	v_pk_fma_f16 v157, v71, v57, v157 op_sel:[1,0,0] op_sel_hi:[1,1,1] neg_lo:[0,0,1] neg_hi:[0,0,1]
	v_pk_fma_f16 v158, v71, v58, v158 op_sel:[1,0,0] op_sel_hi:[1,1,1] neg_lo:[0,0,1] neg_hi:[0,0,1]
	v_pk_fma_f16 v159, v71, v59, v159 op_sel:[1,0,0] op_sel_hi:[1,1,1] neg_lo:[0,0,1] neg_hi:[0,0,1]
	ds_read_b128 v[80:83], v161
	ds_read_b128 v[84:87], v161 offset:1024
	ds_read_b128 v[88:91], v161 offset:2048
	ds_read_b128 v[92:95], v161 offset:3072
	s_waitcnt lgkmcnt(4)
	v_mfma_f32_32x32x16_f16 a[16:31], v[152:155], v[128:131], a[16:31]
	s_waitcnt vmcnt(6)
	v_pk_mul_f16 v144, v48, v32 op_sel:[0,0] op_sel_hi:[0,1]
	v_pk_mul_f16 v145, v48, v33 op_sel:[0,0] op_sel_hi:[0,1]
	v_pk_mul_f16 v146, v48, v34 op_sel:[0,0] op_sel_hi:[0,1]
	v_pk_mul_f16 v147, v48, v35 op_sel:[0,0] op_sel_hi:[0,1]
	v_mfma_f32_32x32x16_f16 a[0:15], v[152:155], v[132:135], a[0:15]
	v_pk_fma_f16 v144, v40, v36, v144 op_sel:[0,0,0] op_sel_hi:[0,1,1]
	v_pk_fma_f16 v145, v40, v37, v145 op_sel:[0,0,0] op_sel_hi:[0,1,1]
	v_pk_fma_f16 v146, v40, v38, v146 op_sel:[0,0,0] op_sel_hi:[0,1,1]
	v_pk_fma_f16 v147, v40, v39, v147 op_sel:[0,0,0] op_sel_hi:[0,1,1]
	v_mfma_f32_32x32x16_f16 a[16:31], v[156:159], v[136:139], a[16:31]
	v_pk_mul_f16 v148, v48, v36 op_sel:[0,0] op_sel_hi:[0,1]
	v_pk_mul_f16 v149, v48, v37 op_sel:[0,0] op_sel_hi:[0,1]
	v_pk_mul_f16 v150, v48, v38 op_sel:[0,0] op_sel_hi:[0,1]
	v_pk_mul_f16 v151, v48, v39 op_sel:[0,0] op_sel_hi:[0,1]
	v_mfma_f32_32x32x16_f16 a[0:15], v[156:159], v[140:143], a[0:15]
	v_pk_fma_f16 v148, v40, v32, v148 op_sel:[0,0,0] op_sel_hi:[0,1,1] neg_lo:[0,0,1] neg_hi:[0,0,1]
	v_pk_fma_f16 v149, v40, v33, v149 op_sel:[0,0,0] op_sel_hi:[0,1,1] neg_lo:[0,0,1] neg_hi:[0,0,1]
	v_pk_fma_f16 v150, v40, v34, v150 op_sel:[0,0,0] op_sel_hi:[0,1,1] neg_lo:[0,0,1] neg_hi:[0,0,1]
	v_pk_fma_f16 v151, v40, v35, v151 op_sel:[0,0,0] op_sel_hi:[0,1,1] neg_lo:[0,0,1] neg_hi:[0,0,1]
	ds_read_b128 v[96:99], v161 offset:4096
	ds_read_b128 v[100:103], v161 offset:5120
	ds_read_b128 v[104:107], v161 offset:6144
	ds_read_b128 v[108:111], v161 offset:7168
	s_add_u32 s17, s17, 1
	s_cmp_eq_u32 s17, 17
	s_cbranch_scc1 .Lk2_epi
	s_branch .Lk2_s00
.Lk2_epi:
	s_waitcnt vmcnt(0) lgkmcnt(0)
	s_nop 15
	s_barrier
	v_accvgpr_read_b32 v0, a0
	v_accvgpr_read_b32 v1, a1
	v_accvgpr_read_b32 v2, a2
	v_accvgpr_read_b32 v3, a3
	v_accvgpr_read_b32 v4, a4
	v_accvgpr_read_b32 v5, a5
	v_accvgpr_read_b32 v6, a6
	v_accvgpr_read_b32 v7, a7
	v_accvgpr_read_b32 v8, a8
	v_accvgpr_read_b32 v9, a9
	v_accvgpr_read_b32 v10, a10
	v_accvgpr_read_b32 v11, a11
	v_accvgpr_read_b32 v12, a12
	v_accvgpr_read_b32 v13, a13
	v_accvgpr_read_b32 v14, a14
	v_accvgpr_read_b32 v15, a15
	v_accvgpr_read_b32 v16, a16
	v_accvgpr_read_b32 v17, a17
	v_accvgpr_read_b32 v18, a18
	v_accvgpr_read_b32 v19, a19
	v_accvgpr_read_b32 v20, a20
	v_accvgpr_read_b32 v21, a21
	v_accvgpr_read_b32 v22, a22
	v_accvgpr_read_b32 v23, a23
	v_accvgpr_read_b32 v24, a24
	v_accvgpr_read_b32 v25, a25
	v_accvgpr_read_b32 v26, a26
	v_accvgpr_read_b32 v27, a27
	v_accvgpr_read_b32 v28, a28
	v_accvgpr_read_b32 v29, a29
	v_accvgpr_read_b32 v30, a30
	v_accvgpr_read_b32 v31, a31
	v_lshlrev_b32_e32 v180, 12, v171
	v_lshlrev_b32_e32 v181, 6, v172
	v_lshlrev_b32_e32 v182, 3, v173
	v_or3_b32 v181, v180, v181, v182
	v_add_u32_e32 v182, 0x800, v181
	v_cvt_pk_f16_f32 v184, v16, v17
	v_cvt_pk_f16_f32 v185, v18, v19
	v_cvt_pk_f16_f32 v186, v20, v21
	v_cvt_pk_f16_f32 v187, v22, v23
	v_cvt_pk_f16_f32 v188, v24, v25
	v_cvt_pk_f16_f32 v189, v26, v27
	v_cvt_pk_f16_f32 v190, v28, v29
	v_cvt_pk_f16_f32 v191, v30, v31
	ds_write2_b64 v181, v[184:185], v[186:187] offset1:2
	ds_write2_b64 v181, v[188:189], v[190:191] offset0:4 offset1:6
	v_cvt_pk_f16_f32 v184, v0, v1
	v_cvt_pk_f16_f32 v185, v2, v3
	v_cvt_pk_f16_f32 v186, v4, v5
	v_cvt_pk_f16_f32 v187, v6, v7
	v_cvt_pk_f16_f32 v188, v8, v9
	v_cvt_pk_f16_f32 v189, v10, v11
	v_cvt_pk_f16_f32 v190, v12, v13
	v_cvt_pk_f16_f32 v191, v14, v15
	ds_write2_b64 v182, v[184:185], v[186:187] offset1:2
	ds_write2_b64 v182, v[188:189], v[190:191] offset0:4 offset1:6
	s_lshl_b32 s36, s10, 18
	s_add_u32 s0, s6, s36
	s_addc_u32 s1, s7, 0
	s_lshl_b32 s36, s11, 3
	s_add_u32 s36, s36, s33
	s_lshl_b32 s36, s36, 12
	s_add_u32 s0, s0, s36
	s_addc_u32 s1, s1, 0
	v_or_b32_e32 v183, v180, v160
	s_waitcnt lgkmcnt(0)
	ds_read_b128 v[0:3], v183
	ds_read_b128 v[4:7], v183 offset:1024
	ds_read_b128 v[8:11], v183 offset:2048
	ds_read_b128 v[12:15], v183 offset:3072
	s_waitcnt lgkmcnt(3)
	global_store_dwordx4 v160, v[0:3], s[0:1] sc0 sc1
	s_waitcnt lgkmcnt(2)
	global_store_dwordx4 v160, v[4:7], s[0:1] offset:1024 sc0 sc1
	s_waitcnt lgkmcnt(1)
	global_store_dwordx4 v160, v[8:11], s[0:1] offset:2048 sc0 sc1
	s_waitcnt lgkmcnt(0)
	global_store_dwordx4 v160, v[12:15], s[0:1] offset:3072 sc0 sc1
	s_endpgm

	.amdhsa_kernel _Z9feat_gemmPKDF16_S0_PDF16_
		.amdhsa_group_segment_fixed_size 114688
		.amdhsa_private_segment_fixed_size 0
		.amdhsa_kernarg_size 24
		.amdhsa_user_sgpr_count 2
		.amdhsa_user_sgpr_dispatch_ptr 0
		.amdhsa_user_sgpr_queue_ptr 0
		.amdhsa_user_sgpr_kernarg_segment_ptr 1
		.amdhsa_user_sgpr_dispatch_id 0
		.amdhsa_user_sgpr_kernarg_preload_length 0
		.amdhsa_user_sgpr_kernarg_preload_offset 0
		.amdhsa_user_sgpr_private_segment_size 0
		.amdhsa_uses_dynamic_stack 0
		.amdhsa_enable_private_segment 0
		.amdhsa_system_sgpr_workgroup_id_x 1
		.amdhsa_system_sgpr_workgroup_id_y 0
		.amdhsa_system_sgpr_workgroup_id_z 0
		.amdhsa_system_sgpr_workgroup_info 0
		.amdhsa_system_vgpr_workitem_id 0
		.amdhsa_next_free_vgpr 224
		.amdhsa_next_free_sgpr 96
		.amdhsa_accum_offset 192
		.amdhsa_reserve_vcc 1
		.amdhsa_float_round_mode_32 0
		.amdhsa_float_round_mode_16_64 0
		.amdhsa_float_denorm_mode_32 3
		.amdhsa_float_denorm_mode_16_64 3
		.amdhsa_dx10_clamp 1
		.amdhsa_ieee_mode 1
		.amdhsa_fp16_overflow 0
		.amdhsa_tg_split 0
		.amdhsa_exception_fp_ieee_invalid_op 0
		.amdhsa_exception_fp_denorm_src 0
		.amdhsa_exception_fp_ieee_div_zero 0
		.amdhsa_exception_fp_ieee_overflow 0
		.amdhsa_exception_fp_ieee_underflow 0
		.amdhsa_exception_fp_ieee_inexact 0
		.amdhsa_exception_int_div_zero 0
	.end_amdhsa_kernel

amdhsa.kernels:
  - .agpr_count:     0
    .args:
      - .actual_access:  read_only
        .address_space:  global
        .offset:         0
        .size:           8
        .value_kind:     global_buffer
      - .actual_access:  read_only
        .address_space:  global
        .offset:         8
        .size:           8
        .value_kind:     global_buffer
      - .actual_access:  write_only
        .address_space:  global
        .offset:         16
        .size:           8
        .value_kind:     global_buffer
      - .actual_access:  read_only
        .address_space:  global
        .offset:         24
        .size:           8
        .value_kind:     global_buffer
      - .actual_access:  write_only
        .address_space:  global
        .offset:         32
        .size:           8
        .value_kind:     global_buffer
    .group_segment_fixed_size: 43008
    .kernarg_segment_align: 8
    .kernarg_segment_size: 40
    .language:       OpenCL C
    .language_version:
      - 2
      - 0
    .max_flat_workgroup_size: 256
    .name:           _Z15sim_prep_kernelPKfS0_PDF16_S0_S1_
    .private_segment_fixed_size: 0
    .sgpr_count:     43
    .sgpr_spill_count: 0
    .symbol:         _Z15sim_prep_kernelPKfS0_PDF16_S0_S1_.kd
    .uniform_work_group_size: 1
    .uses_dynamic_stack: false
    .vgpr_count:     124
    .vgpr_spill_count: 0
    .wavefront_size: 64
  - .agpr_count:     32
    .args:
      - .address_space:  global
        .offset:         0
        .size:           8
        .value_kind:     global_buffer
      - .address_space:  global
        .offset:         8
        .size:           8
        .value_kind:     global_buffer
      - .actual_access:  write_only
        .address_space:  global
        .offset:         16
        .size:           8
        .value_kind:     global_buffer
    .group_segment_fixed_size: 114688
    .kernarg_segment_align: 8
    .kernarg_segment_size: 24
    .language:       OpenCL C
    .language_version:
      - 2
      - 0
    .max_flat_workgroup_size: 512
    .name:           _Z9feat_gemmPKDF16_S0_PDF16_
    .private_segment_fixed_size: 0
    .sgpr_count:     53
    .sgpr_spill_count: 0
    .symbol:         _Z9feat_gemmPKDF16_S0_PDF16_.kd
    .uniform_work_group_size: 1
    .uses_dynamic_stack: false
    .vgpr_count:     224
    .vgpr_spill_count: 0
    .wavefront_size: 64
  - .agpr_count:     0
    .args:
      - .actual_access:  read_only
        .address_space:  global
        .offset:         0
        .size:           8
        .value_kind:     global_buffer
      - .actual_access:  write_only
        .address_space:  global
        .offset:         8
        .size:           8
        .value_kind:     global_buffer
    .group_segment_fixed_size: 0
    .kernarg_segment_align: 8
    .kernarg_segment_size: 16
    .language:       OpenCL C
    .language_version:
      - 2
      - 0
    .max_flat_workgroup_size: 256
    .name:           _Z13reduce_kernelPKDF16_Pf
    .private_segment_fixed_size: 0
    .sgpr_count:     25
    .sgpr_spill_count: 0
    .symbol:         _Z13reduce_kernelPKDF16_Pf.kd
    .uniform_work_group_size: 1
    .uses_dynamic_stack: false
    .vgpr_count:     78
    .vgpr_spill_count: 0
    .wavefront_size: 64
